# baseline (speedup 1.0000x reference)
.LBB0_12:
	v_mov_b32_e32 v46, 1.0
	v_mov_b32_e32 v2, 0
	v_mov_b32_e32 v45, 0
	v_mov_b32_e32 v4, 0
	v_mov_b32_e32 v5, 0
	s_and_saveexec_b64 s[10:11], s[0:1]
	s_cbranch_execz .LBB0_16
	s_and_b64 s[14:15], s[8:9], exec
	s_cselect_b32 s14, 0, 0x208
	v_add_u32_e32 v49, s14, v30
	v_lshl_add_u32 v2, v27, 2, v49
	ds_read_b32 v45, v2 offset:8
	ds_read2_b32 v[4:5], v2 offset1:1
	v_mov_b32_e32 v46, 1.0
	s_waitcnt lgkmcnt(0)
	v_cndmask_b32_e64 v2, v45, -v45, s[2:3]
	v_add_f32_e32 v2, v5, v2
	v_mul_f32_e32 v2, 0.15915494, v2
	v_cos_f32_e32 v5, v2
	v_sin_f32_e32 v47, v2
	v_mov_b32_e32 v45, 0
	v_cmp_gt_f32_e32 vcc, 0, v5
	s_nop 1
	v_cndmask_b32_e32 v2, v43, v44, vcc
	v_cmp_lt_f32_e64 vcc, |v5|, s16
	s_nop 1
	v_cndmask_b32_e32 v2, v5, v2, vcc
	v_div_scale_f32 v5, s[14:15], v2, v2, v47
	v_rcp_f32_e32 v48, v5
	v_div_scale_f32 v50, vcc, v47, v2, v47
	v_fma_f32 v51, -v5, v48, 1.0
	v_fmac_f32_e32 v48, v51, v48
	v_mul_f32_e32 v51, v50, v48
	v_fma_f32 v59, -v5, v51, v50
	v_fmac_f32_e32 v51, v59, v48
	v_fma_f32 v5, -v5, v51, v50
	v_div_fmas_f32 v48, v5, v48, v51
	s_and_saveexec_b64 s[14:15], s[4:5]
	s_cbranch_execz .LBB0_15
	v_lshl_add_u32 v5, v6, 2, v49
	ds_read_b32 v5, v5 offset:96
	s_waitcnt lgkmcnt(0)
	v_mul_f32_e32 v5, 0.5, v5
	v_mul_f32_e32 v5, 0.15915494, v5
	v_cos_f32_e32 v45, v5
	v_sin_f32_e32 v5, v5
	v_cmp_gt_f32_e32 vcc, 0, v45
	s_nop 1
	v_cndmask_b32_e32 v46, v43, v44, vcc
	v_cmp_lt_f32_e64 vcc, |v45|, s16
	s_nop 1
	v_cndmask_b32_e32 v46, v45, v46, vcc
	v_div_scale_f32 v45, s[18:19], v46, v46, v5
	v_rcp_f32_e32 v49, v45
	v_div_scale_f32 v50, vcc, v5, v46, v5
	v_fma_f32 v51, -v45, v49, 1.0
	v_fmac_f32_e32 v49, v51, v49
	v_mul_f32_e32 v51, v50, v49
	v_fma_f32 v59, -v45, v51, v50
	v_fmac_f32_e32 v51, v59, v49
	v_fma_f32 v45, -v45, v51, v50
	v_div_fmas_f32 v45, v45, v49, v51
	v_div_fixup_f32 v45, v45, v46, v5

.LBB0_17:
	s_lshl_b32 s14, s18, 4
	s_lshl_b32 s15, s18, 6
	s_or_b32 s21, s14, 1
	v_or_b32_e32 v48, s15, v31
	v_readlane_b32 s22, v2, s14
	v_or_b32_e32 v49, s15, v32
	v_readlane_b32 s31, v2, s21
	ds_bpermute_b32 v64, v48, v4
	v_or_b32_e32 v50, s15, v33
	v_or_b32_e32 v60, s15, v34
	v_or_b32_e32 v61, s15, v35
	ds_bpermute_b32 v65, v48, v5
	ds_bpermute_b32 v66, v49, v4
	ds_bpermute_b32 v67, v49, v5
	v_mov_b32_e32 v70, s22
	s_waitcnt vmcnt(3)
	v_fma_f32 v85, v70, v54, v58
	s_waitcnt vmcnt(0)
	v_fma_f32 v86, -v70, v3, v55
	v_mov_b32_e32 v87, s31
	v_fma_f32 v3, v70, v55, v3
	v_fma_f32 v54, -v70, v58, v54
	v_fma_f32 v91, v87, v53, v56
	v_fma_f32 v53, -v87, v56, v53
	ds_bpermute_b32 v56, v20, v54
	s_waitcnt lgkmcnt(1)
	v_mul_f32 v98, v64, v66
	v_mul_f32 v64, v64, v67
	v_or_b32_e32 v51, s15, v21
	v_bitop3_b32 v59, s15, 36, v21 bitop3:0x36
	ds_bpermute_b32 v48, v48, v2
	ds_bpermute_b32 v68, v50, v4
	ds_bpermute_b32 v69, v50, v5
	ds_bpermute_b32 v77, v60, v4
	ds_bpermute_b32 v78, v60, v5
	ds_bpermute_b32 v79, v61, v4
	ds_bpermute_b32 v80, v61, v5
	v_fma_f32 v92, -v87, v57, v52
	v_fma_f32 v52, v87, v52, v57
	ds_bpermute_b32 v57, v20, v3
	s_waitcnt lgkmcnt(2)
	v_mul_f32 v99, v77, v79
	v_fma_f32 v67, -v65, v67, v98
	v_fma_f32 v64, v65, v66, v64
	v_fma_f32 v3, v48, v56, v3
	v_or_b32_e32 v62, s15, v22
	s_waitcnt lgkmcnt(1)
	v_fma_f32 v65, -v78, v80, v99
	v_mul_f32 v56, v67, v68
	ds_bpermute_b32 v49, v49, v2
	ds_bpermute_b32 v73, v51, v4 offset:32
	ds_bpermute_b32 v74, v51, v5 offset:32
	ds_bpermute_b32 v75, v59, v4
	ds_bpermute_b32 v76, v59, v5
	ds_bpermute_b32 v94, v20, v53
	ds_bpermute_b32 v95, v20, v52
	v_mul_f32 v77, v77, v80
	s_waitcnt lgkmcnt(1)
	v_fma_f32 v54, -v48, v57, v54
	v_mul_f32 v57, v67, v69
	v_mul_f32 v67, v65, v73
	v_mul_f32 v80, v65, v75
	v_fma_f32 v52, v48, v94, v52
	v_fma_f32 v66, v78, v79, v77
	v_mul_f32 v79, v65, v74
	v_mul_f32 v65, v65, v76
	v_fma_f32 v56, -v64, v69, v56
	ds_swizzle_b32 v69, v52 offset:swizzle(BITMASK_PERM,"piipp")
	ds_bpermute_b32 v81, v62, v4 offset:56
	ds_bpermute_b32 v82, v62, v5 offset:56
	ds_bpermute_b32 v87, v20, v86
	ds_bpermute_b32 v93, v20, v85
	ds_bpermute_b32 v96, v20, v92
	ds_bpermute_b32 v97, v20, v91
	s_waitcnt lgkmcnt(0)
	v_fma_f32 v77, v48, v87, v85
	v_fma_f32 v78, -v48, v93, v86
	v_fma_f32 v85, v48, v96, v91
	v_fma_f32 v86, -v48, v97, v92
	v_fma_f32 v48, -v48, v95, v53
	v_fma_f32 v57, v64, v68, v57
	v_fma_f32 v64, -v66, v74, v67
	v_fma_f32 v67, v66, v73, v79
	v_fma_f32 v68, -v66, v76, v80
	v_fma_f32 v65, v66, v75, v65
	ds_swizzle_b32 v66, v48 offset:swizzle(BITMASK_PERM,"piipp")
	ds_swizzle_b32 v74, v85 offset:swizzle(BITMASK_PERM,"piipp")
	v_readlane_b32 s19, v4, s14
	v_readlane_b32 s20, v5, s14
	v_bitop3_b32 v63, s15, 60, v22 bitop3:0x36
	v_readlane_b32 s29, v4, s21
	v_readlane_b32 s30, v5, s21
	v_mov_b32_e32 v71, s19
	v_mov_b32_e32 v72, s20
	ds_bpermute_b32 v83, v63, v4
	ds_bpermute_b32 v84, v63, v5
	v_mov_b32_e32 v55, s29
	v_mov_b32_e32 v58, s30
	ds_swizzle_b32 v53, v54 offset:swizzle(BITMASK_PERM,"piipp")
	ds_swizzle_b32 v73, v86 offset:swizzle(BITMASK_PERM,"piipp")
	v_mul_f32 v75, v56, v71
	v_mul_f32 v76, v56, v72
	v_mul_f32 v79, v56, v55
	v_mul_f32 v56, v56, v58
	v_mul_f32 v80, v64, v81
	v_mul_f32 v93, v64, v82
	s_waitcnt lgkmcnt(2)
	v_mul_f32 v94, v64, v83
	v_mul_f32 v64, v64, v84
	v_mul_f32 v95, v68, v81
	v_mul_f32 v96, v68, v82
	v_mul_f32 v97, v68, v83
	v_mul_f32 v68, v68, v84
	ds_bpermute_b32 v50, v50, v2
	ds_swizzle_b32 v87, v3 offset:swizzle(BITMASK_PERM,"piipp")
	ds_swizzle_b32 v91, v78 offset:swizzle(BITMASK_PERM,"piipp")
	ds_swizzle_b32 v92, v77 offset:swizzle(BITMASK_PERM,"piipp")
	v_fma_f32 v72, -v57, v72, v75
	v_fma_f32 v71, v57, v71, v76
	v_fma_f32 v58, -v57, v58, v79
	v_fma_f32 v55, v57, v55, v56
	v_fma_f32 v56, -v67, v82, v80
	v_fma_f32 v57, v67, v81, v93
	v_fma_f32 v75, -v67, v84, v94
	v_fma_f32 v64, v67, v83, v64
	v_fma_f32 v67, -v65, v82, v95
	v_fma_f32 v76, v65, v81, v96
	v_fma_f32 v79, -v65, v84, v97
	v_fma_f32 v65, v65, v83, v68
	s_waitcnt lgkmcnt(0)
	v_fma_f32 v68, v49, v91, v77
	v_fma_f32 v77, -v49, v92, v78
	v_fma_f32 v3, v49, v53, v3
	v_fma_f32 v53, -v49, v87, v54
	v_fma_f32 v54, v49, v73, v85
	v_fma_f32 v73, -v49, v74, v86
	v_fma_f32 v52, v49, v66, v52
	v_fma_f32 v48, -v49, v69, v48
	v_mov_b32_dpp v69, v77 quad_perm:[3,2,1,0] row_mask:0xf bank_mask:0xf bound_ctrl:1
	v_mov_b32_dpp v49, v53 quad_perm:[3,2,1,0] row_mask:0xf bank_mask:0xf bound_ctrl:1
	v_mov_b32_dpp v66, v3 quad_perm:[3,2,1,0] row_mask:0xf bank_mask:0xf bound_ctrl:1
	v_mov_b32_dpp v74, v68 quad_perm:[3,2,1,0] row_mask:0xf bank_mask:0xf bound_ctrl:1
	v_mov_b32_dpp v78, v48 quad_perm:[3,2,1,0] row_mask:0xf bank_mask:0xf bound_ctrl:1
	v_mov_b32_dpp v80, v52 quad_perm:[3,2,1,0] row_mask:0xf bank_mask:0xf bound_ctrl:1
	v_mov_b32_dpp v81, v73 quad_perm:[3,2,1,0] row_mask:0xf bank_mask:0xf bound_ctrl:1
	v_mov_b32_dpp v82, v54 quad_perm:[3,2,1,0] row_mask:0xf bank_mask:0xf bound_ctrl:1
	v_fma_f32 v68, v50, v69, v68
	v_fma_f32 v69, -v50, v74, v77
	v_fma_f32 v3, v50, v49, v3
	v_fma_f32 v49, -v50, v66, v53
	v_fma_f32 v53, v50, v81, v54
	v_fma_f32 v54, -v50, v82, v73
	v_fma_f32 v52, v50, v78, v52
	v_fma_f32 v48, -v50, v80, v48
	v_mul_f32 v66, v72, v3
	v_mul_f32 v50, v72, v49
	ds_bpermute_b32 v51, v51, v2 offset:32
	v_fma_f32 v3, -v71, v3, v50
	v_mul_f32 v50, v58, v48
	v_mul_f32 v73, v72, v69
	v_mul_f32 v72, v72, v68
	v_fma_f32 v49, v71, v49, v66
	v_mul_f32 v66, v58, v52
	v_mul_f32 v74, v58, v54
	v_mul_f32 v58, v58, v53
	s_nop 0
	v_fma_f32 v50, -v55, v52, v50
	ds_bpermute_b32 v59, v59, v2
	v_fma_f32 v48, v55, v48, v66
	v_fma_f32 v52, -v55, v53, v74
	v_fma_f32 v53, v55, v54, v58
	ds_bpermute_b32 v54, v19, v3
	ds_bpermute_b32 v55, v19, v49
	v_fma_f32 v68, -v71, v68, v73
	v_fma_f32 v69, v71, v69, v72
	ds_bpermute_b32 v58, v19, v68
	ds_bpermute_b32 v66, v19, v69
	ds_bpermute_b32 v71, v19, v50
	ds_bpermute_b32 v72, v19, v48
	ds_bpermute_b32 v73, v19, v52
	ds_bpermute_b32 v74, v19, v53
	s_waitcnt lgkmcnt(0)
	v_fma_f32 v53, v51, v58, v53
	v_fma_f32 v52, -v51, v66, v52
	v_fma_f32 v48, v59, v54, v48
	v_fma_f32 v50, -v59, v55, v50
	v_fma_f32 v54, v59, v73, v69
	v_fma_f32 v55, -v59, v74, v68
	v_fma_f32 v49, v51, v71, v49
	v_fma_f32 v3, -v51, v72, v3
	ds_swizzle_b32 v51, v50 offset:swizzle(BITMASK_PERM,"iippp")
	ds_bpermute_b32 v60, v60, v2
	ds_swizzle_b32 v58, v48 offset:swizzle(BITMASK_PERM,"iippp")
	ds_swizzle_b32 v59, v52 offset:swizzle(BITMASK_PERM,"iippp")
	ds_swizzle_b32 v66, v53 offset:swizzle(BITMASK_PERM,"iippp")
	ds_swizzle_b32 v68, v3 offset:swizzle(BITMASK_PERM,"iippp")
	ds_swizzle_b32 v69, v49 offset:swizzle(BITMASK_PERM,"iippp")
	ds_swizzle_b32 v71, v55 offset:swizzle(BITMASK_PERM,"iippp")
	ds_swizzle_b32 v72, v54 offset:swizzle(BITMASK_PERM,"iippp")
	s_waitcnt lgkmcnt(0)
	v_fma_f32 v48, v60, v51, v48
	v_fma_f32 v50, -v60, v58, v50
	v_fma_f32 v51, v60, v71, v54
	v_fma_f32 v54, -v60, v72, v55
	ds_swizzle_b32 v55, v50 offset:swizzle(BITMASK_PERM,"ppiip")
	ds_bpermute_b32 v61, v61, v2
	v_fma_f32 v53, v60, v59, v53
	v_fma_f32 v52, -v60, v66, v52
	v_fma_f32 v49, v60, v68, v49
	v_fma_f32 v3, -v60, v69, v3
	ds_swizzle_b32 v58, v48 offset:swizzle(BITMASK_PERM,"ppiip")
	ds_swizzle_b32 v59, v52 offset:swizzle(BITMASK_PERM,"ppiip")
	ds_swizzle_b32 v60, v53 offset:swizzle(BITMASK_PERM,"ppiip")
	ds_swizzle_b32 v66, v3 offset:swizzle(BITMASK_PERM,"ppiip")
	ds_swizzle_b32 v68, v49 offset:swizzle(BITMASK_PERM,"ppiip")
	ds_swizzle_b32 v69, v54 offset:swizzle(BITMASK_PERM,"ppiip")
	ds_bpermute_b32 v62, v62, v2 offset:56
	ds_swizzle_b32 v71, v51 offset:swizzle(BITMASK_PERM,"ppiip")
	s_waitcnt lgkmcnt(0)
	v_fma_f32 v53, v61, v59, v53
	v_fma_f32 v52, -v61, v60, v52
	v_fma_f32 v48, v61, v55, v48
	v_fma_f32 v50, -v61, v58, v50
	v_fma_f32 v51, v61, v69, v51
	v_fma_f32 v54, -v61, v71, v54
	v_fma_f32 v49, v61, v66, v49
	v_fma_f32 v3, -v61, v68, v3
	v_mov_b32_dpp v55, v52 quad_perm:[1,0,3,2] row_mask:0xf bank_mask:0xf bound_ctrl:1
	ds_bpermute_b32 v63, v63, v2
	v_mov_b32_dpp v58, v53 quad_perm:[1,0,3,2] row_mask:0xf bank_mask:0xf bound_ctrl:1
	v_mov_b32_dpp v59, v50 quad_perm:[1,0,3,2] row_mask:0xf bank_mask:0xf bound_ctrl:1
	v_mov_b32_dpp v60, v48 quad_perm:[1,0,3,2] row_mask:0xf bank_mask:0xf bound_ctrl:1
	v_mov_b32_dpp v61, v54 quad_perm:[1,0,3,2] row_mask:0xf bank_mask:0xf bound_ctrl:1
	v_mov_b32_dpp v66, v51 quad_perm:[1,0,3,2] row_mask:0xf bank_mask:0xf bound_ctrl:1
	v_mov_b32_dpp v68, v3 quad_perm:[1,0,3,2] row_mask:0xf bank_mask:0xf bound_ctrl:1
	v_mov_b32_dpp v69, v49 quad_perm:[1,0,3,2] row_mask:0xf bank_mask:0xf bound_ctrl:1
	s_waitcnt lgkmcnt(0)
	v_fma_f32 v51, v63, v59, v51
	v_fma_f32 v54, -v63, v60, v54
	v_fma_f32 v49, v62, v55, v49
	v_fma_f32 v3, -v62, v58, v3
	v_fma_f32 v53, v63, v68, v53
	v_fma_f32 v52, -v63, v69, v52
	v_fma_f32 v48, v62, v61, v48
	v_fma_f32 v50, -v62, v66, v50
	v_mul_f32 v58, v79, v54
	v_mul_f32 v55, v56, v3
	v_mul_f32 v56, v56, v49
	v_mul_f32 v59, v79, v51
	v_mul_f32 v60, v75, v53
	s_or_b32 s23, s14, 3
	v_fma_f32 v49, -v57, v49, v55
	v_fma_f32 v3, v57, v3, v56
	v_mul_f32 v55, v67, v50
	v_mul_f32 v56, v67, v48
	v_mul_f32 v57, v75, v52
	v_fma_f32 v51, -v65, v51, v58
	v_fma_f32 v54, v65, v54, v59
	v_fma_f32 v52, v64, v52, v60
	v_fma_f32 v48, -v76, v48, v55
	v_fma_f32 v50, v76, v50, v56
	v_fma_f32 v53, -v64, v53, v57
	s_or_b32 s24, s14, 2
	v_fmac_f32_dpp v49, v49, v23 quad_perm:[1,0,3,2] row_mask:0xf bank_mask:0xf
	v_fmac_f32_dpp v48, v48, v23 quad_perm:[1,0,3,2] row_mask:0xf bank_mask:0xf
	v_fmac_f32_dpp v53, v53, v23 quad_perm:[1,0,3,2] row_mask:0xf bank_mask:0xf
	v_fmac_f32_dpp v51, v51, v23 quad_perm:[1,0,3,2] row_mask:0xf bank_mask:0xf
	v_fmac_f32_dpp v3, v3, v23 quad_perm:[1,0,3,2] row_mask:0xf bank_mask:0xf
	v_fmac_f32_dpp v50, v50, v23 quad_perm:[1,0,3,2] row_mask:0xf bank_mask:0xf
	v_fmac_f32_dpp v52, v52, v23 quad_perm:[1,0,3,2] row_mask:0xf bank_mask:0xf
	v_fmac_f32_dpp v54, v54, v23 quad_perm:[1,0,3,2] row_mask:0xf bank_mask:0xf

	v_readlane_b32 s20, v45, s23
	s_nop 1
	v_fmac_f32_dpp v49, v49, v24 quad_perm:[2,3,0,1] row_mask:0xf bank_mask:0xf
	v_fmac_f32_dpp v48, v48, v24 quad_perm:[2,3,0,1] row_mask:0xf bank_mask:0xf
	v_fmac_f32_dpp v53, v53, v24 quad_perm:[2,3,0,1] row_mask:0xf bank_mask:0xf
	v_fmac_f32_dpp v51, v51, v24 quad_perm:[2,3,0,1] row_mask:0xf bank_mask:0xf
	v_fmac_f32_dpp v3, v3, v24 quad_perm:[2,3,0,1] row_mask:0xf bank_mask:0xf
	v_fmac_f32_dpp v50, v50, v24 quad_perm:[2,3,0,1] row_mask:0xf bank_mask:0xf
	v_fmac_f32_dpp v52, v52, v24 quad_perm:[2,3,0,1] row_mask:0xf bank_mask:0xf
	v_fmac_f32_dpp v54, v54, v24 quad_perm:[2,3,0,1] row_mask:0xf bank_mask:0xf

	v_readlane_b32 s19, v45, s24
	v_readlane_b32 s15, v45, s14
	v_mov_b32_dpp v55, v49 row_half_mirror row_mask:0xf bank_mask:0xf bound_ctrl:1
	v_mov_b32_dpp v56, v48 row_half_mirror row_mask:0xf bank_mask:0xf bound_ctrl:1
	v_mov_b32_dpp v57, v53 row_half_mirror row_mask:0xf bank_mask:0xf bound_ctrl:1
	v_mov_b32_dpp v58, v51 row_half_mirror row_mask:0xf bank_mask:0xf bound_ctrl:1
	v_mov_b32_dpp v59, v3 row_half_mirror row_mask:0xf bank_mask:0xf bound_ctrl:1
	v_mov_b32_dpp v60, v50 row_half_mirror row_mask:0xf bank_mask:0xf bound_ctrl:1
	v_mov_b32_dpp v61, v52 row_half_mirror row_mask:0xf bank_mask:0xf bound_ctrl:1
	v_mov_b32_dpp v62, v54 row_half_mirror row_mask:0xf bank_mask:0xf bound_ctrl:1
	v_fmac_f32_dpp v49, v55, v25 quad_perm:[3,2,1,0] row_mask:0xf bank_mask:0xf
	v_fmac_f32_dpp v48, v56, v25 quad_perm:[3,2,1,0] row_mask:0xf bank_mask:0xf
	v_fmac_f32_dpp v53, v57, v25 quad_perm:[3,2,1,0] row_mask:0xf bank_mask:0xf
	v_fmac_f32_dpp v51, v58, v25 quad_perm:[3,2,1,0] row_mask:0xf bank_mask:0xf
	v_fmac_f32_dpp v3, v59, v25 quad_perm:[3,2,1,0] row_mask:0xf bank_mask:0xf
	v_fmac_f32_dpp v50, v60, v25 quad_perm:[3,2,1,0] row_mask:0xf bank_mask:0xf
	v_fmac_f32_dpp v52, v61, v25 quad_perm:[3,2,1,0] row_mask:0xf bank_mask:0xf
	v_fmac_f32_dpp v54, v62, v25 quad_perm:[3,2,1,0] row_mask:0xf bank_mask:0xf

	s_or_b32 s25, s14, 4
	v_fmac_f32_dpp v49, v49, v26 row_ror:8 row_mask:0xf bank_mask:0xf
	v_fmac_f32_dpp v48, v48, v26 row_ror:8 row_mask:0xf bank_mask:0xf
	v_fmac_f32_dpp v53, v53, v26 row_ror:8 row_mask:0xf bank_mask:0xf
	v_fmac_f32_dpp v51, v51, v26 row_ror:8 row_mask:0xf bank_mask:0xf
	v_fmac_f32_dpp v3, v3, v26 row_ror:8 row_mask:0xf bank_mask:0xf
	v_fmac_f32_dpp v50, v50, v26 row_ror:8 row_mask:0xf bank_mask:0xf
	v_fmac_f32_dpp v52, v52, v26 row_ror:8 row_mask:0xf bank_mask:0xf
	v_fmac_f32_dpp v54, v54, v26 row_ror:8 row_mask:0xf bank_mask:0xf

	s_or_b32 s26, s14, 5
	v_add_f32 v55, v49, v48
	v_sub_f32 v48, v49, v48
	v_add_f32 v49, v3, v50
	v_sub_f32 v3, v3, v50
	v_add_f32 v50, v53, v51
	v_sub_f32 v51, v53, v51
	v_add_f32 v53, v52, v54
	v_sub_f32 v52, v52, v54
	s_or_b32 s27, s14, 6
	v_add_f32 v54, v55, v50
	v_sub_f32 v50, v55, v50
	v_add_f32 v55, v49, v53
	v_sub_f32 v49, v49, v53
	v_add_f32 v53, v48, v51
	v_sub_f32 v48, v48, v51
	v_add_f32 v51, v3, v52
	v_sub_f32 v3, v3, v52
	s_or_b32 s28, s14, 7
	v_permlane16_swap_b32 v54, v53
	v_permlane16_swap_b32 v55, v51
	v_permlane16_swap_b32 v50, v48
	v_permlane16_swap_b32 v49, v3
	v_readlane_b32 s14, v45, s21
	s_nop 1
	v_permlane32_swap_b32 v54, v50
	v_permlane32_swap_b32 v55, v49
	v_permlane32_swap_b32 v53, v48
	v_permlane32_swap_b32 v51, v3
	v_readlane_b32 s21, v45, s25
	v_add_f32 v52, v54, v53
	v_sub_f32 v53, v54, v53
	v_add_f32 v54, v55, v51
	v_sub_f32 v51, v55, v51
	v_add_f32 v55, v50, v48
	v_sub_f32 v48, v50, v48
	v_add_f32 v50, v49, v3
	v_sub_f32 v3, v49, v3
	v_readlane_b32 s22, v45, s26
	v_add_f32 v49, v52, v55
	v_sub_f32 v52, v52, v55
	v_add_f32 v55, v54, v50
	v_sub_f32 v50, v54, v50
	v_add_f32 v54, v53, v48
	v_sub_f32 v48, v53, v48
	v_add_f32 v53, v51, v3
	v_sub_f32 v3, v51, v3
	v_mul_f32 v49, v49, v7
	v_mul_f32 v51, v55, v7
	v_mul_f32 v54, v54, v8
	v_mul_f32 v48, v48, v10
	v_mul_f32 v53, v53, v8
	v_mul_f32 v3, v3, v10
	v_mul_f32 v52, v52, v9
	v_mul_f32 v50, v50, v9
	s_nop 0
	v_fma_f32 v56, -s20, v54, v51
	v_fma_f32 v51, s20, v51, v54
	v_fma_f32 v55, s20, v53, v49
	v_fma_f32 v49, -s20, v49, v53
	v_fma_f32 v53, s20, v3, v52
	v_fma_f32 v54, -s20, v48, v50
	v_fma_f32 v48, s20, v50, v48
	v_fma_f32 v3, -s20, v52, v3
	v_mov_b32_e32 v70, s21
	v_fma_f32 v50, s19, v54, v55
	v_fma_f32 v52, -s19, v53, v56
	v_fma_f32 v53, s19, v56, v53
	v_fma_f32 v54, -s19, v55, v54
	v_fma_f32 v55, s19, v3, v51
	v_fma_f32 v56, -s19, v48, v49
	v_fma_f32 v48, s19, v49, v48
	v_fma_f32 v3, -s19, v51, v3
	v_readlane_b32 s23, v45, s27
	s_nop 1
	v_permlane32_swap_b32 v50, v53
	v_permlane32_swap_b32 v52, v54
	v_permlane32_swap_b32 v55, v48
	v_permlane32_swap_b32 v56, v3
	v_mov_b32_e32 v88, s22
	s_nop 1
	v_permlane16_swap_b32 v50, v55
	v_permlane16_swap_b32 v52, v56
	v_permlane16_swap_b32 v53, v48
	v_permlane16_swap_b32 v54, v3
	s_and_b64 vcc, exec, s[10:11]
	v_fma_f32 v51, -s14, v55, v52
	v_fma_f32 v58, s14, v52, v55
	v_fma_f32 v52, s14, v3, v53
	v_fma_f32 v55, -s14, v48, v54
	v_fma_f32 v49, s14, v56, v50
	v_fma_f32 v50, -s14, v50, v56
	v_fma_f32 v48, s14, v54, v48
	v_fma_f32 v59, -s14, v53, v3
	s_nop 0
	v_fma_f32 v3, -s15, v52, v51
	v_fma_f32 v52, s15, v51, v52
	v_fma_f32 v54, s15, v55, v49
	v_fma_f32 v56, -s15, v49, v55
	v_fma_f32 v57, -s15, v48, v50
	v_fma_f32 v53, s15, v59, v58
	v_fma_f32 v55, s15, v50, v48
	v_fma_f32 v58, -s15, v58, v59
	s_mov_b64 s[10:11], 0
	v_mul_f32_dpp v48, v54, v70 row_ror:8 row_mask:0xf bank_mask:0xf
	v_mul_f32_dpp v49, v53, v70 row_ror:8 row_mask:0xf bank_mask:0xf
	v_mul_f32_dpp v50, v52, v70 row_ror:8 row_mask:0xf bank_mask:0xf
	v_mul_f32_dpp v51, v55, v70 row_ror:8 row_mask:0xf bank_mask:0xf
	v_fmac_f32_dpp v54, v3, v70 row_ror:8 row_mask:0xf bank_mask:0xf
	v_fmac_f32_dpp v53, v57, v70 row_ror:8 row_mask:0xf bank_mask:0xf
	v_fmac_f32_dpp v52, v56, v70 row_ror:8 row_mask:0xf bank_mask:0xf
	v_fmac_f32_dpp v55, v58, v70 row_ror:8 row_mask:0xf bank_mask:0xf
	v_sub_f32 v3, v3, v48
	v_sub_f32 v57, v57, v49
	v_sub_f32 v56, v56, v50
	v_sub_f32 v58, v58, v51
	s_mov_b32 s18, 1
	v_readlane_b32 s24, v45, s28
	v_mov_b32_dpp v48, v54 row_half_mirror row_mask:0xf bank_mask:0xf bound_ctrl:1
	v_mov_b32_dpp v49, v53 row_half_mirror row_mask:0xf bank_mask:0xf bound_ctrl:1
	v_mov_b32_dpp v50, v52 row_half_mirror row_mask:0xf bank_mask:0xf bound_ctrl:1
	v_mov_b32_dpp v51, v55 row_half_mirror row_mask:0xf bank_mask:0xf bound_ctrl:1
	v_mov_b32_dpp v59, v3 row_half_mirror row_mask:0xf bank_mask:0xf bound_ctrl:1
	v_mov_b32_dpp v60, v57 row_half_mirror row_mask:0xf bank_mask:0xf bound_ctrl:1
	v_mov_b32_dpp v61, v56 row_half_mirror row_mask:0xf bank_mask:0xf bound_ctrl:1
	v_mov_b32_dpp v62, v58 row_half_mirror row_mask:0xf bank_mask:0xf bound_ctrl:1
	v_mul_f32_dpp v63, v48, v88 quad_perm:[3,2,1,0] row_mask:0xf bank_mask:0xf
	v_mul_f32_dpp v64, v49, v88 quad_perm:[3,2,1,0] row_mask:0xf bank_mask:0xf
	v_mul_f32_dpp v65, v50, v88 quad_perm:[3,2,1,0] row_mask:0xf bank_mask:0xf
	v_mul_f32_dpp v66, v51, v88 quad_perm:[3,2,1,0] row_mask:0xf bank_mask:0xf
	v_fmac_f32_dpp v54, v59, v88 quad_perm:[3,2,1,0] row_mask:0xf bank_mask:0xf
	v_fmac_f32_dpp v53, v60, v88 quad_perm:[3,2,1,0] row_mask:0xf bank_mask:0xf
	v_fmac_f32_dpp v52, v61, v88 quad_perm:[3,2,1,0] row_mask:0xf bank_mask:0xf
	v_fmac_f32_dpp v55, v62, v88 quad_perm:[3,2,1,0] row_mask:0xf bank_mask:0xf
	v_sub_f32 v3, v3, v63
	v_sub_f32 v57, v57, v64
	v_sub_f32 v56, v56, v65
	v_sub_f32 v58, v58, v66
	v_mov_b32_e32 v89, s23
	v_mul_f32_dpp v48, v54, v89 quad_perm:[2,3,0,1] row_mask:0xf bank_mask:0xf
	v_mul_f32_dpp v49, v53, v89 quad_perm:[2,3,0,1] row_mask:0xf bank_mask:0xf
	v_mul_f32_dpp v50, v52, v89 quad_perm:[2,3,0,1] row_mask:0xf bank_mask:0xf
	v_mul_f32_dpp v51, v55, v89 quad_perm:[2,3,0,1] row_mask:0xf bank_mask:0xf
	v_fmac_f32_dpp v54, v3, v89 quad_perm:[2,3,0,1] row_mask:0xf bank_mask:0xf
	v_fmac_f32_dpp v53, v57, v89 quad_perm:[2,3,0,1] row_mask:0xf bank_mask:0xf
	v_fmac_f32_dpp v52, v56, v89 quad_perm:[2,3,0,1] row_mask:0xf bank_mask:0xf
	v_fmac_f32_dpp v55, v58, v89 quad_perm:[2,3,0,1] row_mask:0xf bank_mask:0xf
	v_sub_f32 v3, v3, v48
	v_sub_f32 v57, v57, v49
	v_sub_f32 v56, v56, v50
	v_sub_f32 v58, v58, v51
	v_mov_b32_e32 v90, s24
	v_mul_f32_dpp v48, v54, v90 quad_perm:[1,0,3,2] row_mask:0xf bank_mask:0xf
	v_mul_f32_dpp v49, v53, v90 quad_perm:[1,0,3,2] row_mask:0xf bank_mask:0xf
	v_mul_f32_dpp v50, v52, v90 quad_perm:[1,0,3,2] row_mask:0xf bank_mask:0xf
	v_mul_f32_dpp v51, v55, v90 quad_perm:[1,0,3,2] row_mask:0xf bank_mask:0xf
	v_fmac_f32_dpp v54, v3, v90 quad_perm:[1,0,3,2] row_mask:0xf bank_mask:0xf
	v_fmac_f32_dpp v53, v57, v90 quad_perm:[1,0,3,2] row_mask:0xf bank_mask:0xf
	v_fmac_f32_dpp v52, v56, v90 quad_perm:[1,0,3,2] row_mask:0xf bank_mask:0xf
	v_fmac_f32_dpp v55, v58, v90 quad_perm:[1,0,3,2] row_mask:0xf bank_mask:0xf
	v_sub_f32 v3, v3, v48
	v_sub_f32 v57, v57, v49
	v_sub_f32 v56, v56, v50
	v_sub_f32 v58, v58, v51
	s_cbranch_vccnz .LBB0_17
	s_mov_b64 s[10:11], -1
	s_and_b64 vcc, exec, s[8:9]
	v_mul_f32_e32 v2, v46, v47
	v_mul_f32 v51, v54, v2
	v_mul_f32 v50, v3, v2
	v_mul_f32 v49, v53, v2
	v_mul_f32 v48, v57, v2
	v_mul_f32 v47, v52, v2
	v_mul_f32 v46, v56, v2
	v_mul_f32 v45, v55, v2
	v_mul_f32 v5, v58, v2
	s_cbranch_vccz .LBB0_11
	v_mov_b32_e32 v53, 1.0
	v_mov_b32_e32 v55, 0
	v_mov_b32_e32 v4, 0
	v_mov_b32_e32 v52, 0
	v_mov_b32_e32 v2, 0
	v_mov_b32_e32 v3, 0
	s_and_saveexec_b64 s[8:9], s[0:1]
	s_cbranch_execz .LBB0_23
	ds_read_b32 v4, v28 offset:264
	ds_read2_b32 v[2:3], v28 offset0:64 offset1:65
	v_mov_b32_e32 v52, 0
	v_mov_b32_e32 v53, 1.0
	s_waitcnt lgkmcnt(0)
	v_cndmask_b32_e64 v4, v4, -v4, s[2:3]
	v_add_f32_e32 v3, v3, v4
	v_mul_f32_e32 v3, 0.15915494, v3
	v_cos_f32_e32 v4, v3
	v_sin_f32_e32 v54, v3
	v_cmp_gt_f32_e32 vcc, 0, v4
	s_nop 1
	v_cndmask_b32_e32 v3, v43, v44, vcc
	v_cmp_lt_f32_e64 vcc, |v4|, s16
	s_nop 1
	v_cndmask_b32_e32 v4, v4, v3, vcc
	v_div_scale_f32 v3, s[10:11], v4, v4, v54
	v_rcp_f32_e32 v56, v3
	v_div_scale_f32 v57, vcc, v54, v4, v54
	v_fma_f32 v58, -v3, v56, 1.0
	v_fmac_f32_e32 v56, v58, v56
	v_mul_f32_e32 v58, v57, v56
	v_fma_f32 v59, -v3, v58, v57
	v_fmac_f32_e32 v58, v59, v56
	v_fma_f32 v3, -v3, v58, v57
	v_div_fmas_f32 v56, v3, v56, v58
	s_and_saveexec_b64 s[10:11], s[6:7]
	s_cbranch_execz .LBB0_22
	ds_read_b32 v3, v29 offset:352
	s_waitcnt lgkmcnt(0)
	v_mul_f32_e32 v3, 0.5, v3
	v_mul_f32_e32 v3, 0.15915494, v3
	v_cos_f32_e32 v52, v3
	v_sin_f32_e32 v3, v3
	v_cmp_gt_f32_e32 vcc, 0, v52
	s_nop 1
	v_cndmask_b32_e32 v53, v43, v44, vcc
	v_cmp_lt_f32_e64 vcc, |v52|, s16
	s_nop 1
	v_cndmask_b32_e32 v53, v52, v53, vcc
	v_div_scale_f32 v52, s[14:15], v53, v53, v3
	v_rcp_f32_e32 v57, v52
	v_div_scale_f32 v58, vcc, v3, v53, v3
	v_fma_f32 v59, -v52, v57, 1.0
	v_fmac_f32_e32 v57, v59, v57
	v_mul_f32_e32 v59, v58, v57
	v_fma_f32 v60, -v52, v59, v58
	v_fmac_f32_e32 v59, v60, v57
	v_fma_f32 v52, -v52, v59, v58
	v_div_fmas_f32 v52, v52, v57, v59
	v_div_fixup_f32 v52, v52, v53, v3

.LBB0_24:
	s_lshl_b32 s10, s14, 4
	s_lshl_b32 s11, s14, 6
	v_cndmask_b32_e64 v71, 0, 1, s[8:9]
	s_or_b32 s20, s10, 1
	v_or_b32_e32 v73, s11, v36
	v_cmp_ne_u32_e32 vcc, 1, v71
	v_readlane_b32 s28, v4, s10
	v_or_b32_e32 v71, s11, v21
	v_or_b32_e32 v74, s11, v37
	v_readlane_b32 s31, v4, s20
	ds_bpermute_b32 v84, v73, v2
	v_bitop3_b32 v72, s11, 12, v21 bitop3:0x36
	v_or_b32_e32 v75, s11, v38
	v_or_b32_e32 v76, s11, v39
	ds_bpermute_b32 v78, v71, v2 offset:8
	ds_bpermute_b32 v79, v71, v3 offset:8
	ds_bpermute_b32 v80, v71, v4 offset:8
	ds_bpermute_b32 v85, v73, v3
	ds_bpermute_b32 v87, v74, v2
	ds_bpermute_b32 v88, v74, v3
	v_mov_b32_e32 v71, s28
	v_fma_f32 v98, v71, v67, v70
	v_fma_f32 v99, -v71, v68, v69
	v_fma_f32 v100, v71, v65, v64
	v_fma_f32 v101, -v71, v66, v55
	v_mov_b32_e32 v102, s31
	v_fma_f32 v68, v71, v69, v68
	v_fma_f32 v67, -v71, v70, v67
	v_fma_f32 v55, v71, v55, v66
	v_fma_f32 v64, -v71, v64, v65
	v_fma_f32 v107, v102, v60, v63
	v_fma_f32 v109, v102, v56, v59
	v_fma_f32 v110, -v102, v57, v58
	v_fma_f32 v60, -v102, v63, v60
	v_fma_f32 v57, v102, v58, v57
	v_fma_f32 v56, -v102, v59, v56
	ds_bpermute_b32 v58, v19, v67
	ds_bpermute_b32 v59, v19, v68
	ds_bpermute_b32 v63, v19, v55
	s_waitcnt lgkmcnt(3)
	v_mul_f32 v122, v84, v87
	v_mul_f32 v84, v84, v88
	s_or_b32 s21, s10, 8
	s_or_b32 s15, s10, 9
	v_readlane_b32 s27, v3, s10
	v_or_b32_e32 v77, s11, v40
	ds_bpermute_b32 v81, v72, v2
	ds_bpermute_b32 v83, v72, v4
	ds_bpermute_b32 v92, v75, v2
	ds_bpermute_b32 v93, v75, v3
	ds_bpermute_b32 v94, v76, v2
	ds_bpermute_b32 v95, v76, v3
	v_fma_f32 v108, -v102, v61, v62
	v_fma_f32 v61, v102, v62, v61
	ds_bpermute_b32 v62, v19, v64
	s_waitcnt lgkmcnt(2)
	v_mul_f32 v123, v92, v94
	v_fma_f32 v88, -v85, v88, v122
	v_fma_f32 v84, v85, v87, v84
	v_fma_f32 v63, -v83, v63, v67
	v_fma_f32 v55, v80, v58, v55
	v_fma_f32 v58, -v80, v59, v64
	s_waitcnt lgkmcnt(1)
	v_fma_f32 v85, -v93, v95, v123
	v_mul_f32 v59, v88, v78
	v_mul_f32 v64, v88, v79
	v_mul_f32 v67, v88, v81
	v_readlane_b32 s19, v2, s10
	v_readlane_b32 s29, v2, s20
	v_readlane_b32 s30, v3, s20
	ds_bpermute_b32 v82, v72, v3
	v_mov_b32_e32 v91, s27
	v_readlane_b32 s27, v2, s21
	v_readlane_b32 s28, v2, s15
	v_readlane_b32 s33, v3, s21
	v_readlane_b32 s34, v3, s15
	ds_bpermute_b32 v96, v77, v2
	ds_bpermute_b32 v97, v77, v3
	ds_bpermute_b32 v112, v19, v101
	ds_bpermute_b32 v113, v19, v100
	ds_bpermute_b32 v114, v19, v60
	ds_bpermute_b32 v115, v19, v61
	ds_bpermute_b32 v116, v19, v56
	ds_bpermute_b32 v117, v19, v57
	ds_bpermute_b32 v118, v19, v108
	ds_bpermute_b32 v119, v19, v107
	ds_bpermute_b32 v120, v19, v110
	v_mul_f32 v92, v92, v95
	s_waitcnt lgkmcnt(9)
	v_fma_f32 v62, v83, v62, v68
	v_mul_f32 v68, v88, v82
	v_mul_f32 v88, v85, v96
	v_mul_f32 v85, v85, v97
	v_fma_f32 v59, -v84, v79, v59
	v_fma_f32 v87, v93, v94, v92
	v_fma_f32 v64, v84, v78, v64
	v_fma_f32 v67, -v84, v82, v67
	ds_bpermute_b32 v86, v73, v4
	v_fma_f32 v78, -v87, v97, v88
	v_mov_b32_e32 v90, s19
	v_mov_b32_e32 v65, s29
	v_mov_b32_e32 v66, s30
	v_mov_b32_e32 v103, s27
	v_mov_b32_e32 v104, s33
	v_mov_b32_e32 v105, s28
	v_mov_b32_e32 v106, s34
	ds_bpermute_b32 v102, v19, v99
	ds_bpermute_b32 v111, v19, v98
	ds_bpermute_b32 v121, v19, v109
	s_waitcnt lgkmcnt(0)
	v_fma_f32 v92, v83, v112, v98
	v_fma_f32 v93, -v83, v113, v99
	v_fma_f32 v94, v80, v102, v100
	v_fma_f32 v95, -v80, v111, v101
	v_fma_f32 v98, v83, v120, v107
	v_fma_f32 v99, -v83, v121, v108
	v_fma_f32 v100, v80, v118, v109
	v_fma_f32 v101, -v80, v119, v110
	v_fma_f32 v61, v83, v116, v61
	v_fma_f32 v60, -v83, v117, v60
	v_fma_f32 v57, v80, v114, v57
	v_fma_f32 v56, -v80, v115, v56
	ds_swizzle_b32 v80, v58 offset:swizzle(BITMASK_PERM,"iippp")
	ds_swizzle_b32 v83, v55 offset:swizzle(BITMASK_PERM,"iippp")
	v_fma_f32 v68, v84, v81, v68
	v_fma_f32 v79, v87, v96, v85
	ds_swizzle_b32 v81, v56 offset:swizzle(BITMASK_PERM,"iippp")
	ds_swizzle_b32 v82, v57 offset:swizzle(BITMASK_PERM,"iippp")
	ds_swizzle_b32 v84, v60 offset:swizzle(BITMASK_PERM,"iippp")
	ds_swizzle_b32 v85, v61 offset:swizzle(BITMASK_PERM,"iippp")
	ds_swizzle_b32 v87, v101 offset:swizzle(BITMASK_PERM,"iippp")
	ds_swizzle_b32 v88, v100 offset:swizzle(BITMASK_PERM,"iippp")
	v_mul_f32 v112, v59, v90
	v_mul_f32 v113, v59, v91
	v_mul_f32 v114, v59, v65
	v_mul_f32 v59, v59, v66
	v_mul_f32 v115, v67, v90
	v_mul_f32 v116, v67, v91
	v_mul_f32 v117, v67, v65
	v_mul_f32 v67, v67, v66
	v_mul_f32 v118, v78, v103
	v_mul_f32 v119, v78, v104
	v_mul_f32 v120, v78, v105
	v_mul_f32 v78, v78, v106
	ds_swizzle_b32 v102, v63 offset:swizzle(BITMASK_PERM,"iippp")
	ds_swizzle_b32 v107, v62 offset:swizzle(BITMASK_PERM,"iippp")
	ds_swizzle_b32 v108, v95 offset:swizzle(BITMASK_PERM,"iippp")
	ds_swizzle_b32 v109, v94 offset:swizzle(BITMASK_PERM,"iippp")
	ds_swizzle_b32 v110, v93 offset:swizzle(BITMASK_PERM,"iippp")
	ds_swizzle_b32 v111, v92 offset:swizzle(BITMASK_PERM,"iippp")
	ds_swizzle_b32 v96, v99 offset:swizzle(BITMASK_PERM,"iippp")
	ds_swizzle_b32 v97, v98 offset:swizzle(BITMASK_PERM,"iippp")
	v_fma_f32 v112, -v64, v91, v112
	v_fma_f32 v113, v64, v90, v113
	v_fma_f32 v114, -v64, v66, v114
	v_fma_f32 v59, v64, v65, v59
	v_fma_f32 v64, -v68, v91, v115
	v_fma_f32 v90, v68, v90, v116
	v_fma_f32 v66, -v68, v66, v117
	v_fma_f32 v65, v68, v65, v67
	v_fma_f32 v67, -v79, v104, v118
	v_fma_f32 v68, v79, v103, v119
	v_fma_f32 v91, -v79, v106, v120
	v_fma_f32 v78, v79, v105, v78
	s_waitcnt lgkmcnt(2)
	v_fma_f32 v79, v86, v110, v92
	v_fma_f32 v92, -v86, v111, v93
	v_fma_f32 v93, v86, v108, v94
	v_fma_f32 v94, -v86, v109, v95
	v_fma_f32 v62, v86, v102, v62
	v_fma_f32 v63, -v86, v107, v63
	v_fma_f32 v55, v86, v80, v55
	v_fma_f32 v58, -v86, v83, v58
	s_waitcnt lgkmcnt(0)
	v_fma_f32 v80, v86, v96, v98
	v_fma_f32 v83, -v86, v97, v99
	v_fma_f32 v87, v86, v87, v100
	v_fma_f32 v88, -v86, v88, v101
	v_fma_f32 v61, v86, v84, v61
	v_fma_f32 v60, -v86, v85, v60
	v_fma_f32 v57, v86, v81, v57
	v_fma_f32 v56, -v86, v82, v56
	ds_swizzle_b32 v81, v58 offset:swizzle(BITMASK_PERM,"ppiip")
	ds_swizzle_b32 v82, v55 offset:swizzle(BITMASK_PERM,"ppiip")
	ds_swizzle_b32 v84, v63 offset:swizzle(BITMASK_PERM,"ppiip")
	ds_swizzle_b32 v85, v62 offset:swizzle(BITMASK_PERM,"ppiip")
	ds_swizzle_b32 v86, v94 offset:swizzle(BITMASK_PERM,"ppiip")
	ds_swizzle_b32 v95, v93 offset:swizzle(BITMASK_PERM,"ppiip")
	ds_bpermute_b32 v89, v74, v4
	v_readlane_b32 s35, v4, s21
	v_readlane_b32 s36, v4, s15
	ds_swizzle_b32 v96, v92 offset:swizzle(BITMASK_PERM,"ppiip")
	ds_swizzle_b32 v97, v79 offset:swizzle(BITMASK_PERM,"ppiip")
	ds_swizzle_b32 v98, v56 offset:swizzle(BITMASK_PERM,"ppiip")
	ds_swizzle_b32 v99, v57 offset:swizzle(BITMASK_PERM,"ppiip")
	ds_swizzle_b32 v100, v60 offset:swizzle(BITMASK_PERM,"ppiip")
	ds_swizzle_b32 v101, v61 offset:swizzle(BITMASK_PERM,"ppiip")
	ds_swizzle_b32 v102, v88 offset:swizzle(BITMASK_PERM,"ppiip")
	ds_swizzle_b32 v103, v87 offset:swizzle(BITMASK_PERM,"ppiip")
	ds_swizzle_b32 v104, v83 offset:swizzle(BITMASK_PERM,"ppiip")
	ds_swizzle_b32 v105, v80 offset:swizzle(BITMASK_PERM,"ppiip")
	s_waitcnt lgkmcnt(8)
	v_fma_f32 v79, v89, v96, v79
	v_fma_f32 v92, -v89, v97, v92
	v_fma_f32 v86, v89, v86, v93
	v_fma_f32 v93, -v89, v95, v94
	v_fma_f32 v62, v89, v84, v62
	v_fma_f32 v63, -v89, v85, v63
	v_fma_f32 v55, v89, v81, v55
	v_fma_f32 v58, -v89, v82, v58
	s_waitcnt lgkmcnt(0)
	v_fma_f32 v80, v89, v104, v80
	v_fma_f32 v81, -v89, v105, v83
	v_fma_f32 v82, v89, v102, v87
	v_fma_f32 v83, -v89, v103, v88
	v_fma_f32 v61, v89, v100, v61
	v_fma_f32 v60, -v89, v101, v60
	v_fma_f32 v57, v89, v98, v57
	v_fma_f32 v56, -v89, v99, v56
	v_mul_f32 v84, v112, v58
	v_mul_f32 v85, v112, v55
	v_mul_f32 v87, v64, v63
	v_mul_f32 v88, v64, v62
	v_mul_f32 v95, v64, v92
	v_mul_f32 v64, v64, v79
	v_mov_b32_e32 v69, s35
	v_mov_b32_e32 v70, s36
	v_mul_f32 v89, v112, v93
	v_mul_f32 v94, v112, v86
	v_fma_f32 v55, -v113, v55, v84
	v_fma_f32 v58, v113, v58, v85
	v_fma_f32 v62, -v90, v62, v87
	v_fma_f32 v63, v90, v63, v88
	v_mul_f32 v84, v114, v56
	v_mul_f32 v85, v114, v57
	v_mul_f32 v87, v66, v60
	v_mul_f32 v88, v66, v61
	v_mul_f32 v96, v114, v83
	v_mul_f32 v97, v114, v82
	v_mul_f32 v98, v66, v81
	v_mul_f32 v66, v66, v80
	v_fma_f32 v86, -v113, v86, v89
	v_fma_f32 v79, -v90, v79, v95
	v_fma_f32 v64, v90, v92, v64
	v_fma_f32 v57, -v59, v57, v84
	v_fma_f32 v56, v59, v56, v85
	v_fma_f32 v61, -v65, v61, v87
	v_fma_f32 v60, v65, v60, v88
	v_fma_f32 v82, -v59, v82, v96
	v_fma_f32 v59, v59, v83, v97
	v_fma_f32 v80, -v65, v80, v98
	v_fma_f32 v65, v65, v81, v66
	ds_bpermute_b32 v75, v75, v4
	v_fma_f32 v89, v113, v93, v94
	v_fma_f32 v66, v69, v82, v64
	v_fma_f32 v81, -v69, v59, v79
	v_fma_f32 v84, -v70, v65, v86
	v_fma_f32 v65, v70, v86, v65
	v_fma_f32 v59, v69, v79, v59
	v_fma_f32 v83, v70, v80, v89
	v_fma_f32 v80, -v70, v89, v80
	v_fma_f32 v64, -v69, v64, v82
	v_fma_f32 v79, v69, v55, v60
	v_fma_f32 v82, -v69, v58, v61
	v_fma_f32 v85, v70, v62, v56
	v_fma_f32 v86, -v70, v63, v57
	v_fma_f32 v57, v70, v57, v63
	v_fma_f32 v56, -v70, v56, v62
	v_fma_f32 v58, v69, v61, v58
	v_fma_f32 v55, -v69, v60, v55
	ds_bpermute_b32 v60, v20, v55
	ds_bpermute_b32 v61, v20, v58
	ds_bpermute_b32 v62, v20, v56
	ds_bpermute_b32 v63, v20, v57
	ds_bpermute_b32 v69, v20, v86
	ds_bpermute_b32 v70, v20, v85
	ds_bpermute_b32 v87, v20, v82
	ds_bpermute_b32 v92, v20, v80
	ds_bpermute_b32 v88, v20, v79
	ds_bpermute_b32 v89, v20, v64
	ds_bpermute_b32 v90, v20, v59
	ds_bpermute_b32 v93, v20, v81
	ds_bpermute_b32 v94, v20, v66
	ds_bpermute_b32 v95, v20, v84
	ds_bpermute_b32 v96, v20, v83
	ds_bpermute_b32 v97, v20, v65
	s_waitcnt lgkmcnt(0)
	v_fma_f32 v66, v75, v93, v66
	v_fma_f32 v81, -v75, v94, v81
	v_fma_f32 v83, v75, v95, v83
	v_fma_f32 v84, -v75, v96, v84
	v_fma_f32 v65, v75, v92, v65
	v_fma_f32 v80, -v75, v97, v80
	v_fma_f32 v59, v75, v89, v59
	v_fma_f32 v64, -v75, v90, v64
	v_fma_f32 v79, v75, v87, v79
	v_fma_f32 v82, -v75, v88, v82
	v_fma_f32 v69, v75, v69, v85
	v_fma_f32 v70, -v75, v70, v86
	v_fma_f32 v57, v75, v62, v57
	v_fma_f32 v56, -v75, v63, v56
	v_fma_f32 v58, v75, v60, v58
	v_fma_f32 v55, -v75, v61, v55
	ds_swizzle_b32 v60, v55 offset:swizzle(BITMASK_PERM,"piipp")
	ds_swizzle_b32 v61, v58 offset:swizzle(BITMASK_PERM,"piipp")
	ds_swizzle_b32 v62, v56 offset:swizzle(BITMASK_PERM,"piipp")
	ds_swizzle_b32 v63, v57 offset:swizzle(BITMASK_PERM,"piipp")
	ds_swizzle_b32 v75, v70 offset:swizzle(BITMASK_PERM,"piipp")
	ds_swizzle_b32 v85, v69 offset:swizzle(BITMASK_PERM,"piipp")
	ds_swizzle_b32 v86, v82 offset:swizzle(BITMASK_PERM,"piipp")
	ds_swizzle_b32 v87, v79 offset:swizzle(BITMASK_PERM,"piipp")
	ds_swizzle_b32 v92, v81 offset:swizzle(BITMASK_PERM,"piipp")
	ds_bpermute_b32 v76, v76, v4
	ds_swizzle_b32 v88, v64 offset:swizzle(BITMASK_PERM,"piipp")
	ds_swizzle_b32 v89, v59 offset:swizzle(BITMASK_PERM,"piipp")
	ds_swizzle_b32 v90, v80 offset:swizzle(BITMASK_PERM,"piipp")
	ds_swizzle_b32 v93, v66 offset:swizzle(BITMASK_PERM,"piipp")
	ds_swizzle_b32 v94, v84 offset:swizzle(BITMASK_PERM,"piipp")
	ds_swizzle_b32 v95, v83 offset:swizzle(BITMASK_PERM,"piipp")
	ds_bpermute_b32 v77, v77, v4
	ds_swizzle_b32 v96, v65 offset:swizzle(BITMASK_PERM,"piipp")
	s_waitcnt lgkmcnt(0)
	v_fma_f32 v66, v76, v92, v66
	v_fma_f32 v81, -v76, v93, v81
	v_fma_f32 v83, v76, v94, v83
	v_fma_f32 v84, -v76, v95, v84
	v_fma_f32 v65, v76, v90, v65
	v_fma_f32 v80, -v76, v96, v80
	v_fma_f32 v59, v76, v88, v59
	v_fma_f32 v64, -v76, v89, v64
	v_fma_f32 v79, v76, v86, v79
	v_fma_f32 v82, -v76, v87, v82
	v_fma_f32 v69, v76, v75, v69
	v_fma_f32 v70, -v76, v85, v70
	v_fma_f32 v57, v76, v62, v57
	v_fma_f32 v56, -v76, v63, v56
	v_fma_f32 v58, v76, v60, v58
	v_fma_f32 v55, -v76, v61, v55
	s_nop 1
	v_mov_b32_dpp v85, v82 quad_perm:[3,2,1,0] row_mask:0xf bank_mask:0xf bound_ctrl:1
	v_mov_b32_dpp v75, v70 quad_perm:[3,2,1,0] row_mask:0xf bank_mask:0xf bound_ctrl:1
	v_mov_b32_dpp v60, v55 quad_perm:[3,2,1,0] row_mask:0xf bank_mask:0xf bound_ctrl:1
	v_mov_b32_dpp v61, v58 quad_perm:[3,2,1,0] row_mask:0xf bank_mask:0xf bound_ctrl:1
	v_mov_b32_dpp v62, v56 quad_perm:[3,2,1,0] row_mask:0xf bank_mask:0xf bound_ctrl:1
	v_mov_b32_dpp v63, v57 quad_perm:[3,2,1,0] row_mask:0xf bank_mask:0xf bound_ctrl:1
	v_mov_b32_dpp v86, v79 quad_perm:[3,2,1,0] row_mask:0xf bank_mask:0xf bound_ctrl:1
	v_mov_b32_dpp v87, v64 quad_perm:[3,2,1,0] row_mask:0xf bank_mask:0xf bound_ctrl:1
	v_mov_b32_dpp v92, v84 quad_perm:[3,2,1,0] row_mask:0xf bank_mask:0xf bound_ctrl:1
	v_mov_b32_dpp v76, v69 quad_perm:[3,2,1,0] row_mask:0xf bank_mask:0xf bound_ctrl:1
	v_mov_b32_dpp v88, v59 quad_perm:[3,2,1,0] row_mask:0xf bank_mask:0xf bound_ctrl:1
	v_mov_b32_dpp v89, v80 quad_perm:[3,2,1,0] row_mask:0xf bank_mask:0xf bound_ctrl:1
	v_mov_b32_dpp v90, v65 quad_perm:[3,2,1,0] row_mask:0xf bank_mask:0xf bound_ctrl:1
	v_mov_b32_dpp v93, v83 quad_perm:[3,2,1,0] row_mask:0xf bank_mask:0xf bound_ctrl:1
	v_mov_b32_dpp v94, v81 quad_perm:[3,2,1,0] row_mask:0xf bank_mask:0xf bound_ctrl:1
	v_mov_b32_dpp v95, v66 quad_perm:[3,2,1,0] row_mask:0xf bank_mask:0xf bound_ctrl:1
	v_fma_f32 v66, v77, v94, v66
	v_fma_f32 v81, -v77, v95, v81
	v_fma_f32 v83, v77, v92, v83
	v_fma_f32 v84, -v77, v93, v84
	v_fma_f32 v65, v77, v89, v65
	v_fma_f32 v80, -v77, v90, v80
	v_fma_f32 v59, v77, v87, v59
	v_fma_f32 v64, -v77, v88, v64
	v_fma_f32 v79, v77, v85, v79
	v_fma_f32 v82, -v77, v86, v82
	v_fma_f32 v69, v77, v75, v69
	v_fma_f32 v70, -v77, v76, v70
	v_fma_f32 v57, v77, v62, v57
	v_fma_f32 v56, -v77, v63, v56
	v_fma_f32 v58, v77, v60, v58
	v_fma_f32 v55, -v77, v61, v55
	v_mul_f32 v77, v67, v82
	v_mul_f32 v75, v91, v70
	v_mul_f32 v63, v91, v57
	v_mul_f32 v62, v91, v56
	v_mul_f32 v61, v67, v58
	v_mul_f32 v60, v67, v55
	v_mul_f32 v85, v67, v79
	v_mul_f32 v86, v67, v64
	v_mul_f32 v87, v67, v59
	v_mul_f32 v92, v67, v81
	v_mul_f32 v67, v67, v66
	v_mul_f32 v76, v91, v69
	v_mul_f32 v88, v91, v80
	v_mul_f32 v89, v91, v65
	v_mul_f32 v90, v91, v84
	v_mul_f32 v91, v91, v83
	v_fma_f32 v58, -v68, v58, v60
	v_fma_f32 v55, v68, v55, v61
	v_fma_f32 v57, -v78, v57, v62
	v_fma_f32 v56, v78, v56, v63
	v_fma_f32 v60, -v78, v69, v75
	v_fma_f32 v61, v78, v70, v76
	v_fma_f32 v62, -v68, v79, v77
	v_fma_f32 v63, v68, v82, v85
	v_fma_f32 v59, -v68, v59, v86
	v_fma_f32 v64, v68, v64, v87
	v_fma_f32 v65, -v78, v65, v88
	v_fma_f32 v69, v78, v80, v89
	v_fma_f32 v70, -v78, v83, v90
	v_fma_f32 v75, v78, v84, v91
	v_fma_f32 v66, -v68, v66, v92
	v_fma_f32 v67, v68, v81, v67
	s_nop 0
	s_nop 1
	v_fmac_f32_dpp v58, v58, v23 quad_perm:[1,0,3,2] row_mask:0xf bank_mask:0xf
	v_fmac_f32_dpp v57, v57, v23 quad_perm:[1,0,3,2] row_mask:0xf bank_mask:0xf
	v_fmac_f32_dpp v60, v60, v23 quad_perm:[1,0,3,2] row_mask:0xf bank_mask:0xf
	v_fmac_f32_dpp v62, v62, v23 quad_perm:[1,0,3,2] row_mask:0xf bank_mask:0xf
	v_fmac_f32_dpp v55, v55, v23 quad_perm:[1,0,3,2] row_mask:0xf bank_mask:0xf
	v_fmac_f32_dpp v56, v56, v23 quad_perm:[1,0,3,2] row_mask:0xf bank_mask:0xf
	v_fmac_f32_dpp v61, v61, v23 quad_perm:[1,0,3,2] row_mask:0xf bank_mask:0xf
	v_fmac_f32_dpp v63, v63, v23 quad_perm:[1,0,3,2] row_mask:0xf bank_mask:0xf

	s_or_b32 s18, s10, 4
	v_fmac_f32_dpp v59, v59, v23 quad_perm:[1,0,3,2] row_mask:0xf bank_mask:0xf
	v_fmac_f32_dpp v65, v65, v23 quad_perm:[1,0,3,2] row_mask:0xf bank_mask:0xf
	v_fmac_f32_dpp v70, v70, v23 quad_perm:[1,0,3,2] row_mask:0xf bank_mask:0xf
	v_fmac_f32_dpp v66, v66, v23 quad_perm:[1,0,3,2] row_mask:0xf bank_mask:0xf
	v_fmac_f32_dpp v64, v64, v23 quad_perm:[1,0,3,2] row_mask:0xf bank_mask:0xf
	v_fmac_f32_dpp v69, v69, v23 quad_perm:[1,0,3,2] row_mask:0xf bank_mask:0xf
	v_fmac_f32_dpp v75, v75, v23 quad_perm:[1,0,3,2] row_mask:0xf bank_mask:0xf
	v_fmac_f32_dpp v67, v67, v23 quad_perm:[1,0,3,2] row_mask:0xf bank_mask:0xf

	v_fmac_f32_dpp v58, v58, v24 quad_perm:[2,3,0,1] row_mask:0xf bank_mask:0xf
	v_fmac_f32_dpp v57, v57, v24 quad_perm:[2,3,0,1] row_mask:0xf bank_mask:0xf
	v_fmac_f32_dpp v60, v60, v24 quad_perm:[2,3,0,1] row_mask:0xf bank_mask:0xf
	v_fmac_f32_dpp v62, v62, v24 quad_perm:[2,3,0,1] row_mask:0xf bank_mask:0xf
	v_fmac_f32_dpp v55, v55, v24 quad_perm:[2,3,0,1] row_mask:0xf bank_mask:0xf
	v_fmac_f32_dpp v56, v56, v24 quad_perm:[2,3,0,1] row_mask:0xf bank_mask:0xf
	v_fmac_f32_dpp v61, v61, v24 quad_perm:[2,3,0,1] row_mask:0xf bank_mask:0xf
	v_fmac_f32_dpp v63, v63, v24 quad_perm:[2,3,0,1] row_mask:0xf bank_mask:0xf

	s_or_b32 s22, s10, 3
	v_fmac_f32_dpp v59, v59, v24 quad_perm:[2,3,0,1] row_mask:0xf bank_mask:0xf
	v_fmac_f32_dpp v65, v65, v24 quad_perm:[2,3,0,1] row_mask:0xf bank_mask:0xf
	v_fmac_f32_dpp v70, v70, v24 quad_perm:[2,3,0,1] row_mask:0xf bank_mask:0xf
	v_fmac_f32_dpp v66, v66, v24 quad_perm:[2,3,0,1] row_mask:0xf bank_mask:0xf
	v_fmac_f32_dpp v64, v64, v24 quad_perm:[2,3,0,1] row_mask:0xf bank_mask:0xf
	v_fmac_f32_dpp v69, v69, v24 quad_perm:[2,3,0,1] row_mask:0xf bank_mask:0xf
	v_fmac_f32_dpp v75, v75, v24 quad_perm:[2,3,0,1] row_mask:0xf bank_mask:0xf
	v_fmac_f32_dpp v67, v67, v24 quad_perm:[2,3,0,1] row_mask:0xf bank_mask:0xf

	v_readlane_b32 s19, v52, s18
	v_mov_b32_dpp v68, v58 row_half_mirror row_mask:0xf bank_mask:0xf bound_ctrl:1
	v_mov_b32_dpp v76, v57 row_half_mirror row_mask:0xf bank_mask:0xf bound_ctrl:1
	v_mov_b32_dpp v77, v60 row_half_mirror row_mask:0xf bank_mask:0xf bound_ctrl:1
	v_mov_b32_dpp v78, v62 row_half_mirror row_mask:0xf bank_mask:0xf bound_ctrl:1
	v_mov_b32_dpp v79, v55 row_half_mirror row_mask:0xf bank_mask:0xf bound_ctrl:1
	v_mov_b32_dpp v80, v56 row_half_mirror row_mask:0xf bank_mask:0xf bound_ctrl:1
	v_mov_b32_dpp v81, v61 row_half_mirror row_mask:0xf bank_mask:0xf bound_ctrl:1
	v_mov_b32_dpp v82, v63 row_half_mirror row_mask:0xf bank_mask:0xf bound_ctrl:1
	v_mov_b32_dpp v83, v59 row_half_mirror row_mask:0xf bank_mask:0xf bound_ctrl:1
	v_mov_b32_dpp v84, v65 row_half_mirror row_mask:0xf bank_mask:0xf bound_ctrl:1
	v_mov_b32_dpp v85, v70 row_half_mirror row_mask:0xf bank_mask:0xf bound_ctrl:1
	v_mov_b32_dpp v86, v66 row_half_mirror row_mask:0xf bank_mask:0xf bound_ctrl:1
	v_mov_b32_dpp v87, v64 row_half_mirror row_mask:0xf bank_mask:0xf bound_ctrl:1
	v_mov_b32_dpp v88, v69 row_half_mirror row_mask:0xf bank_mask:0xf bound_ctrl:1
	v_mov_b32_dpp v89, v75 row_half_mirror row_mask:0xf bank_mask:0xf bound_ctrl:1
	v_mov_b32_dpp v90, v67 row_half_mirror row_mask:0xf bank_mask:0xf bound_ctrl:1
	v_fmac_f32_dpp v58, v68, v25 quad_perm:[3,2,1,0] row_mask:0xf bank_mask:0xf
	v_fmac_f32_dpp v57, v76, v25 quad_perm:[3,2,1,0] row_mask:0xf bank_mask:0xf
	v_fmac_f32_dpp v60, v77, v25 quad_perm:[3,2,1,0] row_mask:0xf bank_mask:0xf
	v_fmac_f32_dpp v62, v78, v25 quad_perm:[3,2,1,0] row_mask:0xf bank_mask:0xf
	v_fmac_f32_dpp v55, v79, v25 quad_perm:[3,2,1,0] row_mask:0xf bank_mask:0xf
	v_fmac_f32_dpp v56, v80, v25 quad_perm:[3,2,1,0] row_mask:0xf bank_mask:0xf
	v_fmac_f32_dpp v61, v81, v25 quad_perm:[3,2,1,0] row_mask:0xf bank_mask:0xf
	v_fmac_f32_dpp v63, v82, v25 quad_perm:[3,2,1,0] row_mask:0xf bank_mask:0xf

	v_fmac_f32_dpp v59, v83, v25 quad_perm:[3,2,1,0] row_mask:0xf bank_mask:0xf
	v_fmac_f32_dpp v65, v84, v25 quad_perm:[3,2,1,0] row_mask:0xf bank_mask:0xf
	v_fmac_f32_dpp v70, v85, v25 quad_perm:[3,2,1,0] row_mask:0xf bank_mask:0xf
	v_fmac_f32_dpp v66, v86, v25 quad_perm:[3,2,1,0] row_mask:0xf bank_mask:0xf
	v_fmac_f32_dpp v64, v87, v25 quad_perm:[3,2,1,0] row_mask:0xf bank_mask:0xf
	v_fmac_f32_dpp v69, v88, v25 quad_perm:[3,2,1,0] row_mask:0xf bank_mask:0xf
	v_fmac_f32_dpp v75, v89, v25 quad_perm:[3,2,1,0] row_mask:0xf bank_mask:0xf
	v_fmac_f32_dpp v67, v90, v25 quad_perm:[3,2,1,0] row_mask:0xf bank_mask:0xf

	v_readlane_b32 s18, v52, s22
	s_nop 1
	v_fmac_f32_dpp v58, v58, v26 row_ror:8 row_mask:0xf bank_mask:0xf
	v_fmac_f32_dpp v57, v57, v26 row_ror:8 row_mask:0xf bank_mask:0xf
	v_fmac_f32_dpp v60, v60, v26 row_ror:8 row_mask:0xf bank_mask:0xf
	v_fmac_f32_dpp v62, v62, v26 row_ror:8 row_mask:0xf bank_mask:0xf
	v_fmac_f32_dpp v55, v55, v26 row_ror:8 row_mask:0xf bank_mask:0xf
	v_fmac_f32_dpp v56, v56, v26 row_ror:8 row_mask:0xf bank_mask:0xf
	v_fmac_f32_dpp v61, v61, v26 row_ror:8 row_mask:0xf bank_mask:0xf
	v_fmac_f32_dpp v63, v63, v26 row_ror:8 row_mask:0xf bank_mask:0xf

	v_fmac_f32_dpp v59, v59, v26 row_ror:8 row_mask:0xf bank_mask:0xf
	v_fmac_f32_dpp v65, v65, v26 row_ror:8 row_mask:0xf bank_mask:0xf
	v_fmac_f32_dpp v70, v70, v26 row_ror:8 row_mask:0xf bank_mask:0xf
	v_fmac_f32_dpp v66, v66, v26 row_ror:8 row_mask:0xf bank_mask:0xf
	v_fmac_f32_dpp v64, v64, v26 row_ror:8 row_mask:0xf bank_mask:0xf
	v_fmac_f32_dpp v69, v69, v26 row_ror:8 row_mask:0xf bank_mask:0xf
	v_fmac_f32_dpp v75, v75, v26 row_ror:8 row_mask:0xf bank_mask:0xf
	v_fmac_f32_dpp v67, v67, v26 row_ror:8 row_mask:0xf bank_mask:0xf

	s_or_b32 s23, s10, 2
	v_add_f32 v68, v58, v57
	v_sub_f32 v57, v58, v57
	v_add_f32 v58, v55, v56
	v_sub_f32 v55, v55, v56
	v_add_f32 v56, v60, v62
	v_sub_f32 v60, v60, v62
	v_add_f32 v62, v61, v63
	v_sub_f32 v61, v61, v63
	v_add_f32 v63, v59, v65
	v_sub_f32 v59, v59, v65
	v_add_f32 v65, v64, v69
	v_sub_f32 v64, v64, v69
	v_add_f32 v69, v70, v66
	v_sub_f32 v66, v70, v66
	v_add_f32 v70, v75, v67
	v_sub_f32 v67, v75, v67
	v_add_f32 v75, v68, v56
	v_sub_f32 v56, v68, v56
	v_add_f32 v68, v58, v62
	v_sub_f32 v58, v58, v62
	v_add_f32 v62, v57, v60
	v_sub_f32 v57, v57, v60
	v_add_f32 v60, v55, v61
	v_sub_f32 v55, v55, v61
	v_add_f32 v61, v63, v69
	v_sub_f32 v63, v63, v69
	v_add_f32 v69, v65, v70
	v_sub_f32 v65, v65, v70
	v_add_f32 v70, v59, v66
	v_sub_f32 v59, v59, v66
	v_add_f32 v66, v64, v67
	v_sub_f32 v64, v64, v67
	v_add_f32 v67, v75, v61
	v_sub_f32 v61, v75, v61
	v_add_f32 v75, v68, v69
	v_sub_f32 v68, v68, v69
	v_add_f32 v69, v62, v70
	v_sub_f32 v62, v62, v70
	v_add_f32 v70, v60, v66
	v_sub_f32 v60, v60, v66
	v_add_f32 v66, v56, v63
	v_sub_f32 v56, v56, v63
	v_add_f32 v63, v58, v65
	v_sub_f32 v58, v58, v65
	v_add_f32 v65, v57, v59
	v_sub_f32 v57, v57, v59
	v_add_f32 v59, v55, v64
	v_sub_f32 v55, v55, v64
	v_readlane_b32 s15, v52, s23
	s_nop 1
	v_permlane16_swap_b32 v67, v69
	v_permlane16_swap_b32 v75, v70
	v_permlane16_swap_b32 v66, v65
	v_permlane16_swap_b32 v63, v59
	v_permlane16_swap_b32 v61, v62
	v_permlane16_swap_b32 v68, v60
	v_permlane16_swap_b32 v56, v57
	v_permlane16_swap_b32 v58, v55
	s_or_b32 s24, s10, 5
	v_permlane32_swap_b32 v67, v66
	v_permlane32_swap_b32 v75, v63
	v_permlane32_swap_b32 v69, v65
	v_permlane32_swap_b32 v70, v59
	v_permlane32_swap_b32 v61, v56
	v_permlane32_swap_b32 v68, v58
	v_permlane32_swap_b32 v62, v57
	v_permlane32_swap_b32 v60, v55
	v_readlane_b32 s11, v52, s20
	v_add_f32 v64, v67, v69
	v_sub_f32 v67, v67, v69
	v_add_f32 v69, v75, v70
	v_sub_f32 v70, v75, v70
	v_add_f32 v75, v66, v65
	v_sub_f32 v65, v66, v65
	v_add_f32 v66, v63, v59
	v_sub_f32 v59, v63, v59
	v_add_f32 v63, v61, v62
	v_sub_f32 v61, v61, v62
	v_add_f32 v62, v68, v60
	v_sub_f32 v60, v68, v60
	v_add_f32 v68, v56, v57
	v_sub_f32 v56, v56, v57
	v_add_f32 v57, v58, v55
	v_sub_f32 v55, v58, v55
	v_add_f32 v58, v64, v75
	v_sub_f32 v64, v64, v75
	v_add_f32 v75, v69, v66
	v_sub_f32 v66, v69, v66
	v_add_f32 v69, v67, v65
	v_sub_f32 v65, v67, v65
	v_add_f32 v67, v70, v59
	v_sub_f32 v59, v70, v59
	v_add_f32 v70, v63, v68
	v_sub_f32 v63, v63, v68
	v_add_f32 v68, v62, v57
	v_sub_f32 v57, v62, v57
	v_add_f32 v62, v61, v56
	v_sub_f32 v56, v61, v56
	v_add_f32 v61, v60, v55
	v_sub_f32 v55, v60, v55
	v_mul_f32 v58, v58, v11
	v_mul_f32 v60, v75, v11
	v_mul_f32 v69, v69, v12
	v_mul_f32 v67, v67, v12
	v_mul_f32 v64, v64, v13
	v_mul_f32 v66, v66, v13
	v_mul_f32 v65, v65, v14
	v_mul_f32 v59, v59, v14
	v_mul_f32 v70, v70, v15
	v_mul_f32 v68, v68, v15
	v_mul_f32 v62, v62, v16
	v_mul_f32 v61, v61, v16
	v_mul_f32 v56, v56, v18
	v_mul_f32 v55, v55, v18
	v_mul_f32 v63, v63, v17
	v_mul_f32 v57, v57, v17
	s_nop 0
	v_fma_f32 v75, s19, v67, v58
	v_fma_f32 v76, -s19, v69, v60
	v_fma_f32 v60, s19, v60, v69
	v_fma_f32 v58, -s19, v58, v67
	v_fma_f32 v67, s19, v59, v64
	v_fma_f32 v69, -s19, v65, v66
	v_fma_f32 v65, s19, v66, v65
	v_fma_f32 v59, -s19, v64, v59
	v_fma_f32 v64, s19, v61, v70
	v_fma_f32 v66, -s19, v62, v68
	v_fma_f32 v62, s19, v68, v62
	v_fma_f32 v61, -s19, v70, v61
	v_fma_f32 v68, s19, v55, v63
	v_fma_f32 v70, -s19, v56, v57
	v_fma_f32 v56, s19, v57, v56
	v_fma_f32 v55, -s19, v63, v55
	s_nop 0
	v_fma_f32 v57, s18, v69, v75
	v_fma_f32 v63, -s18, v67, v76
	v_fma_f32 v67, s18, v76, v67
	v_fma_f32 v69, -s18, v75, v69
	v_fma_f32 v75, s18, v59, v60
	v_fma_f32 v76, -s18, v65, v58
	v_fma_f32 v58, s18, v58, v65
	v_fma_f32 v59, -s18, v60, v59
	v_fma_f32 v60, s18, v70, v64
	v_fma_f32 v65, -s18, v68, v66
	v_fma_f32 v66, s18, v66, v68
	v_fma_f32 v64, -s18, v64, v70
	v_fma_f32 v68, s18, v55, v62
	v_fma_f32 v70, -s18, v56, v61
	v_fma_f32 v56, s18, v61, v56
	v_fma_f32 v55, -s18, v62, v55
	s_nop 0
	s_nop 1
	v_permlane32_swap_b32 v57, v67
	v_permlane32_swap_b32 v63, v69
	v_permlane32_swap_b32 v75, v58
	v_permlane32_swap_b32 v76, v59
	s_or_b32 s25, s10, 6
	v_permlane32_swap_b32 v60, v66
	v_permlane32_swap_b32 v65, v64
	v_permlane32_swap_b32 v68, v56
	v_permlane32_swap_b32 v70, v55
	v_permlane16_swap_b32 v57, v75
	v_permlane16_swap_b32 v63, v76
	v_permlane16_swap_b32 v67, v58
	v_permlane16_swap_b32 v69, v59
	s_or_b32 s26, s10, 7
	v_permlane16_swap_b32 v60, v68
	v_permlane16_swap_b32 v65, v70
	v_permlane16_swap_b32 v66, v56
	v_permlane16_swap_b32 v64, v55
	v_fma_f32 v61, s15, v76, v57
	v_fma_f32 v62, -s15, v75, v63
	v_fma_f32 v63, s15, v63, v75
	v_fma_f32 v57, -s15, v57, v76
	v_fma_f32 v75, s15, v59, v67
	v_fma_f32 v76, -s15, v58, v69
	v_fma_f32 v58, s15, v69, v58
	v_fma_f32 v59, -s15, v67, v59
	s_nop 0
	v_fma_f32 v67, s15, v70, v60
	v_fma_f32 v69, -s15, v68, v65
	v_fma_f32 v60, -s15, v60, v70
	v_fma_f32 v70, -s15, v56, v64
	v_fma_f32 v65, s15, v65, v68
	v_fma_f32 v68, s15, v55, v66
	v_fma_f32 v56, s15, v64, v56
	v_fma_f32 v55, -s15, v66, v55
	v_fma_f32 v64, s11, v76, v61
	v_fma_f32 v77, -s11, v75, v62
	v_fma_f32 v75, s11, v62, v75
	v_fma_f32 v61, -s11, v61, v76
	v_fma_f32 v76, s11, v59, v63
	v_fma_f32 v62, -s11, v58, v57
	v_fma_f32 v78, s11, v57, v58
	v_fma_f32 v79, -s11, v63, v59
	s_nop 0
	v_fma_f32 v57, s11, v70, v67
	v_fma_f32 v59, -s11, v68, v69
	v_fma_f32 v69, s11, v69, v68
	v_fma_f32 v70, -s11, v67, v70
	v_fma_f32 v63, s11, v55, v65
	v_readlane_b32 s10, v52, s10
	v_readlane_b32 s20, v52, s24
	v_fma_f32 v80, -s11, v56, v60
	v_fma_f32 v81, s11, v60, v56
	v_fma_f32 v82, -s11, v65, v55
	v_fma_f32 v65, s10, v59, v64
	v_fma_f32 v66, -s10, v57, v77
	v_fma_f32 v58, s10, v77, v57
	v_fma_f32 v59, -s10, v64, v59
	s_nop 0
	v_fma_f32 v67, s10, v80, v76
	v_fma_f32 v68, -s10, v63, v62
	v_fma_f32 v62, s10, v62, v63
	v_fma_f32 v63, -s10, v76, v80
	v_fma_f32 v56, s10, v70, v75
	v_fma_f32 v57, -s10, v69, v61
	v_fma_f32 v55, s10, v61, v69
	v_fma_f32 v64, -s10, v75, v70
	v_fma_f32 v60, s10, v82, v78
	v_fma_f32 v61, -s10, v81, v79
	v_fma_f32 v69, s10, v79, v81
	v_fma_f32 v70, -s10, v78, v82
	s_nop 0
	v_mov_b32_e32 v74, s20
	s_nop 1
	v_mul_f32_dpp v75, v65, v74 row_ror:8 row_mask:0xf bank_mask:0xf
	v_mul_f32_dpp v76, v67, v74 row_ror:8 row_mask:0xf bank_mask:0xf
	v_mul_f32_dpp v77, v56, v74 row_ror:8 row_mask:0xf bank_mask:0xf
	v_mul_f32_dpp v78, v60, v74 row_ror:8 row_mask:0xf bank_mask:0xf
	v_fmac_f32_dpp v65, v66, v74 row_ror:8 row_mask:0xf bank_mask:0xf
	v_fmac_f32_dpp v67, v68, v74 row_ror:8 row_mask:0xf bank_mask:0xf
	v_fmac_f32_dpp v56, v57, v74 row_ror:8 row_mask:0xf bank_mask:0xf
	v_fmac_f32_dpp v60, v61, v74 row_ror:8 row_mask:0xf bank_mask:0xf
	v_sub_f32 v66, v66, v75
	v_sub_f32 v68, v68, v76
	v_sub_f32 v57, v57, v77
	v_sub_f32 v61, v61, v78
	v_readlane_b32 s22, v52, s25
	s_nop 1
	v_mul_f32_dpp v75, v58, v74 row_ror:8 row_mask:0xf bank_mask:0xf
	v_mul_f32_dpp v76, v62, v74 row_ror:8 row_mask:0xf bank_mask:0xf
	v_mul_f32_dpp v77, v55, v74 row_ror:8 row_mask:0xf bank_mask:0xf
	v_mul_f32_dpp v78, v69, v74 row_ror:8 row_mask:0xf bank_mask:0xf
	v_fmac_f32_dpp v58, v59, v74 row_ror:8 row_mask:0xf bank_mask:0xf
	v_fmac_f32_dpp v62, v63, v74 row_ror:8 row_mask:0xf bank_mask:0xf
	v_fmac_f32_dpp v55, v64, v74 row_ror:8 row_mask:0xf bank_mask:0xf
	v_fmac_f32_dpp v69, v70, v74 row_ror:8 row_mask:0xf bank_mask:0xf
	v_sub_f32 v59, v59, v75
	v_sub_f32 v63, v63, v76
	v_sub_f32 v64, v64, v77
	v_sub_f32 v70, v70, v78
	v_readlane_b32 s23, v52, s26
	v_mov_b32_dpp v74, v65 row_half_mirror row_mask:0xf bank_mask:0xf bound_ctrl:1
	v_mov_b32_dpp v75, v67 row_half_mirror row_mask:0xf bank_mask:0xf bound_ctrl:1
	v_mov_b32_dpp v76, v56 row_half_mirror row_mask:0xf bank_mask:0xf bound_ctrl:1
	v_mov_b32_dpp v77, v60 row_half_mirror row_mask:0xf bank_mask:0xf bound_ctrl:1
	v_mov_b32_e32 v73, s22
	v_mov_b32_dpp v78, v66 row_half_mirror row_mask:0xf bank_mask:0xf bound_ctrl:1
	v_mov_b32_dpp v79, v68 row_half_mirror row_mask:0xf bank_mask:0xf bound_ctrl:1
	v_mov_b32_dpp v80, v57 row_half_mirror row_mask:0xf bank_mask:0xf bound_ctrl:1
	v_mov_b32_dpp v81, v61 row_half_mirror row_mask:0xf bank_mask:0xf bound_ctrl:1
	v_mov_b32_dpp v82, v58 row_half_mirror row_mask:0xf bank_mask:0xf bound_ctrl:1
	v_mov_b32_dpp v83, v62 row_half_mirror row_mask:0xf bank_mask:0xf bound_ctrl:1
	v_mov_b32_dpp v84, v55 row_half_mirror row_mask:0xf bank_mask:0xf bound_ctrl:1
	v_mov_b32_dpp v85, v69 row_half_mirror row_mask:0xf bank_mask:0xf bound_ctrl:1
	v_mov_b32_dpp v86, v59 row_half_mirror row_mask:0xf bank_mask:0xf bound_ctrl:1
	v_mov_b32_dpp v87, v63 row_half_mirror row_mask:0xf bank_mask:0xf bound_ctrl:1
	v_mov_b32_dpp v88, v64 row_half_mirror row_mask:0xf bank_mask:0xf bound_ctrl:1
	v_mov_b32_dpp v89, v70 row_half_mirror row_mask:0xf bank_mask:0xf bound_ctrl:1
	v_mul_f32_dpp v90, v74, v73 quad_perm:[3,2,1,0] row_mask:0xf bank_mask:0xf
	v_mul_f32_dpp v91, v75, v73 quad_perm:[3,2,1,0] row_mask:0xf bank_mask:0xf
	v_mul_f32_dpp v92, v76, v73 quad_perm:[3,2,1,0] row_mask:0xf bank_mask:0xf
	v_mul_f32_dpp v93, v77, v73 quad_perm:[3,2,1,0] row_mask:0xf bank_mask:0xf
	v_fmac_f32_dpp v65, v78, v73 quad_perm:[3,2,1,0] row_mask:0xf bank_mask:0xf
	v_fmac_f32_dpp v67, v79, v73 quad_perm:[3,2,1,0] row_mask:0xf bank_mask:0xf
	v_fmac_f32_dpp v56, v80, v73 quad_perm:[3,2,1,0] row_mask:0xf bank_mask:0xf
	v_fmac_f32_dpp v60, v81, v73 quad_perm:[3,2,1,0] row_mask:0xf bank_mask:0xf
	v_sub_f32 v66, v66, v90
	v_sub_f32 v68, v68, v91
	v_sub_f32 v57, v57, v92
	v_sub_f32 v61, v61, v93
	v_mul_f32_dpp v74, v82, v73 quad_perm:[3,2,1,0] row_mask:0xf bank_mask:0xf
	v_mul_f32_dpp v75, v83, v73 quad_perm:[3,2,1,0] row_mask:0xf bank_mask:0xf
	v_mul_f32_dpp v76, v84, v73 quad_perm:[3,2,1,0] row_mask:0xf bank_mask:0xf
	v_mul_f32_dpp v77, v85, v73 quad_perm:[3,2,1,0] row_mask:0xf bank_mask:0xf
	v_fmac_f32_dpp v58, v86, v73 quad_perm:[3,2,1,0] row_mask:0xf bank_mask:0xf
	v_fmac_f32_dpp v62, v87, v73 quad_perm:[3,2,1,0] row_mask:0xf bank_mask:0xf
	v_fmac_f32_dpp v55, v88, v73 quad_perm:[3,2,1,0] row_mask:0xf bank_mask:0xf
	v_fmac_f32_dpp v69, v89, v73 quad_perm:[3,2,1,0] row_mask:0xf bank_mask:0xf
	v_sub_f32 v59, v59, v74
	v_sub_f32 v63, v63, v75
	v_sub_f32 v64, v64, v76
	v_sub_f32 v70, v70, v77
	s_mov_b64 s[8:9], 0
	s_mov_b32 s14, 1
	v_readlane_b32 s21, v52, s21
	s_and_b64 vcc, exec, vcc
	v_mov_b32_e32 v72, s23
	s_nop 1
	v_mul_f32_dpp v73, v65, v72 quad_perm:[2,3,0,1] row_mask:0xf bank_mask:0xf
	v_mul_f32_dpp v74, v67, v72 quad_perm:[2,3,0,1] row_mask:0xf bank_mask:0xf
	v_mul_f32_dpp v75, v56, v72 quad_perm:[2,3,0,1] row_mask:0xf bank_mask:0xf
	v_mul_f32_dpp v76, v60, v72 quad_perm:[2,3,0,1] row_mask:0xf bank_mask:0xf
	v_fmac_f32_dpp v65, v66, v72 quad_perm:[2,3,0,1] row_mask:0xf bank_mask:0xf
	v_fmac_f32_dpp v67, v68, v72 quad_perm:[2,3,0,1] row_mask:0xf bank_mask:0xf
	v_fmac_f32_dpp v56, v57, v72 quad_perm:[2,3,0,1] row_mask:0xf bank_mask:0xf
	v_fmac_f32_dpp v60, v61, v72 quad_perm:[2,3,0,1] row_mask:0xf bank_mask:0xf
	v_sub_f32 v66, v66, v73
	v_sub_f32 v68, v68, v74
	v_sub_f32 v57, v57, v75
	v_sub_f32 v61, v61, v76
	v_mov_b32_e32 v71, s21
	v_mul_f32_dpp v73, v58, v72 quad_perm:[2,3,0,1] row_mask:0xf bank_mask:0xf
	v_mul_f32_dpp v74, v62, v72 quad_perm:[2,3,0,1] row_mask:0xf bank_mask:0xf
	v_mul_f32_dpp v75, v55, v72 quad_perm:[2,3,0,1] row_mask:0xf bank_mask:0xf
	v_mul_f32_dpp v76, v69, v72 quad_perm:[2,3,0,1] row_mask:0xf bank_mask:0xf
	v_fmac_f32_dpp v58, v59, v72 quad_perm:[2,3,0,1] row_mask:0xf bank_mask:0xf
	v_fmac_f32_dpp v62, v63, v72 quad_perm:[2,3,0,1] row_mask:0xf bank_mask:0xf
	v_fmac_f32_dpp v55, v64, v72 quad_perm:[2,3,0,1] row_mask:0xf bank_mask:0xf
	v_fmac_f32_dpp v69, v70, v72 quad_perm:[2,3,0,1] row_mask:0xf bank_mask:0xf
	v_sub_f32 v59, v59, v73
	v_sub_f32 v63, v63, v74
	v_sub_f32 v64, v64, v75
	v_sub_f32 v70, v70, v76
	s_nop 0
	s_nop 1
	v_mul_f32_dpp v72, v65, v71 quad_perm:[1,0,3,2] row_mask:0xf bank_mask:0xf
	v_mul_f32_dpp v73, v67, v71 quad_perm:[1,0,3,2] row_mask:0xf bank_mask:0xf
	v_mul_f32_dpp v74, v56, v71 quad_perm:[1,0,3,2] row_mask:0xf bank_mask:0xf
	v_mul_f32_dpp v75, v60, v71 quad_perm:[1,0,3,2] row_mask:0xf bank_mask:0xf
	v_fmac_f32_dpp v65, v66, v71 quad_perm:[1,0,3,2] row_mask:0xf bank_mask:0xf
	v_fmac_f32_dpp v67, v68, v71 quad_perm:[1,0,3,2] row_mask:0xf bank_mask:0xf
	v_fmac_f32_dpp v56, v57, v71 quad_perm:[1,0,3,2] row_mask:0xf bank_mask:0xf
	v_fmac_f32_dpp v60, v61, v71 quad_perm:[1,0,3,2] row_mask:0xf bank_mask:0xf
	v_sub_f32 v66, v66, v72
	v_sub_f32 v68, v68, v73
	v_sub_f32 v57, v57, v74
	v_sub_f32 v61, v61, v75
	s_nop 0
	s_nop 1
	v_mul_f32_dpp v72, v58, v71 quad_perm:[1,0,3,2] row_mask:0xf bank_mask:0xf
	v_mul_f32_dpp v73, v62, v71 quad_perm:[1,0,3,2] row_mask:0xf bank_mask:0xf
	v_mul_f32_dpp v74, v55, v71 quad_perm:[1,0,3,2] row_mask:0xf bank_mask:0xf
	v_mul_f32_dpp v75, v69, v71 quad_perm:[1,0,3,2] row_mask:0xf bank_mask:0xf
	v_fmac_f32_dpp v58, v59, v71 quad_perm:[1,0,3,2] row_mask:0xf bank_mask:0xf
	v_fmac_f32_dpp v62, v63, v71 quad_perm:[1,0,3,2] row_mask:0xf bank_mask:0xf
	v_fmac_f32_dpp v55, v64, v71 quad_perm:[1,0,3,2] row_mask:0xf bank_mask:0xf
	v_fmac_f32_dpp v69, v70, v71 quad_perm:[1,0,3,2] row_mask:0xf bank_mask:0xf
	v_sub_f32 v59, v59, v72
	v_sub_f32 v63, v63, v73
	v_sub_f32 v64, v64, v74
	v_sub_f32 v70, v70, v75
	s_cbranch_vccz .LBB0_24
	v_mul_f32_e32 v2, v53, v54
	v_mul_f32 v3, v65, v2
	v_mul_f32 v55, v57, v2
	v_mul_f32 v4, v66, v2
	v_mul_f32 v52, v67, v2
	v_mul_f32 v53, v68, v2
	v_mul_f32 v54, v56, v2
	v_mul_f32 v57, v3, v3
	v_mul_f32 v56, v60, v2
	v_mul_f32 v2, v61, v2
	s_mov_b64 s[10:11], 0
	v_fma_f32 v57, v4, v4, v57
	s_nop 0
	v_fma_f32 v57, v52, v52, v57
	s_nop 0
	v_fma_f32 v57, v53, v53, v57
	s_nop 0
	v_fma_f32 v57, v54, v54, v57
	s_nop 0
	v_fma_f32 v57, v55, v55, v57
	s_nop 0
	v_fma_f32 v57, v56, v56, v57
	s_nop 0
	v_fma_f32 v57, v2, v2, v57
	s_nop 1
	v_add_f32_dpp v57, v57, v57 quad_perm:[1,0,3,2] row_mask:0xf bank_mask:0xf bound_ctrl:1
	s_nop 1
	v_add_f32_dpp v57, v57, v57 quad_perm:[2,3,0,1] row_mask:0xf bank_mask:0xf bound_ctrl:1
	ds_swizzle_b32 v58, v57 offset:swizzle(SWAP,4)
	s_waitcnt lgkmcnt(0)
	v_add_f32_e32 v57, v57, v58
	s_nop 1
	v_add_f32_dpp v57, v57, v57 row_ror:8 row_mask:0xf bank_mask:0xf bound_ctrl:1
	ds_swizzle_b32 v58, v57 offset:swizzle(SWAP,16)
	s_waitcnt lgkmcnt(0)
	v_add_f32_e32 v57, v57, v58
	ds_bpermute_b32 v58, v19, v57
	s_waitcnt lgkmcnt(0)
	v_add_f32_e32 v57, v57, v58
	v_mul_f32_e32 v58, 0x4f800000, v57
	v_cmp_gt_f32_e32 vcc, s17, v57
	s_nop 1
	v_cndmask_b32_e32 v57, v57, v58, vcc
	v_sqrt_f32_e32 v58, v57
	s_nop 0
	v_add_u32_e32 v59, -1, v58
	v_add_u32_e32 v60, 1, v58
	v_fma_f32 v61, -v59, v58, v57
	v_fma_f32 v62, -v60, v58, v57
	v_cmp_ge_f32_e64 s[8:9], 0, v61
	s_nop 1
	v_cndmask_b32_e64 v58, v58, v59, s[8:9]
	v_cmp_lt_f32_e64 s[8:9], 0, v62
	s_nop 1
	v_cndmask_b32_e64 v58, v58, v60, s[8:9]
	v_mul_f32_e32 v59, 0x37800000, v58
	v_cndmask_b32_e32 v58, v58, v59, vcc
	v_cmp_class_f32_e32 vcc, v57, v41
	s_nop 1
	v_cndmask_b32_e32 v57, v58, v57, vcc
	v_add_f32_e32 v57, 0x322bcc77, v57
	v_div_scale_f32 v58, s[8:9], v57, v57, 1.0
	v_rcp_f32_e32 v59, v58
	v_div_scale_f32 v60, vcc, 1.0, v57, 1.0
	v_fma_f32 v61, -v58, v59, 1.0
	v_fmac_f32_e32 v59, v61, v59
	v_mul_f32_e32 v61, v60, v59
	v_fma_f32 v62, -v58, v61, v60
	v_fmac_f32_e32 v61, v62, v59
	v_fma_f32 v58, -v58, v61, v60
	v_div_fmas_f32 v58, v58, v59, v61
	v_div_fixup_f32 v57, v58, v57, 1.0
	v_mul_f32 v3, v3, v57
	v_mul_f32 v4, v4, v57
	v_mul_f32 v52, v52, v57
	v_mul_f32 v53, v53, v57
	v_mul_f32 v2, v2, v57
	s_nop 0
	v_mul_f32 v58, v3, v42
	s_nop 0
	v_max_f32 v3, v3, v58
	v_mul_f32 v58, v4, v42
	s_nop 0
	v_max_f32 v4, v4, v58
	v_mul_f32 v58, v52, v42
	s_nop 0
	v_max_f32 v52, v52, v58
	v_mul_f32 v58, v53, v42
	s_nop 0
	v_max_f32 v58, v53, v58
	v_mul_f32 v53, v54, v57
	v_mul_f32 v54, v55, v57
	s_nop 0
	v_mul_f32 v55, v53, v42
	s_nop 0
	v_max_f32 v55, v53, v55
	v_mul_f32 v53, v54, v42
	s_nop 0
	v_max_f32 v59, v54, v53
	v_mul_f32 v53, v56, v57
	s_nop 0
	v_mul_f32 v54, v53, v42
	s_nop 0
	v_max_f32 v60, v53, v54
	v_mul_f32 v53, v2, v42
	s_nop 0
	v_max_f32 v2, v2, v53
	v_mul_f32 v53, v3, v3
	s_nop 0
	v_fma_f32 v53, v4, v4, v53
	s_nop 0
	v_fma_f32 v53, v52, v52, v53
	s_nop 0
	v_fma_f32 v53, v58, v58, v53
	s_nop 0
	v_fma_f32 v53, v55, v55, v53
	s_nop 0
	v_fma_f32 v53, v59, v59, v53
	s_nop 0
	v_fma_f32 v53, v60, v60, v53
	s_nop 0
	v_fma_f32 v53, v2, v2, v53
	s_nop 1
	v_add_f32_dpp v53, v53, v53 quad_perm:[1,0,3,2] row_mask:0xf bank_mask:0xf bound_ctrl:1
	s_nop 1
	v_add_f32_dpp v53, v53, v53 quad_perm:[2,3,0,1] row_mask:0xf bank_mask:0xf bound_ctrl:1
	ds_swizzle_b32 v54, v53 offset:swizzle(SWAP,4)
	s_waitcnt lgkmcnt(0)
	v_add_f32_e32 v53, v53, v54
	s_nop 1
	v_add_f32_dpp v53, v53, v53 row_ror:8 row_mask:0xf bank_mask:0xf bound_ctrl:1
	ds_swizzle_b32 v54, v53 offset:swizzle(SWAP,16)
	s_waitcnt lgkmcnt(0)
	v_add_f32_e32 v53, v53, v54
	ds_bpermute_b32 v54, v19, v53
	s_waitcnt lgkmcnt(0)
	v_add_f32_e32 v53, v53, v54
	v_mul_f32_e32 v54, 0x4f800000, v53
	v_cmp_gt_f32_e32 vcc, s17, v53
	s_nop 1
	v_cndmask_b32_e32 v53, v53, v54, vcc
	v_sqrt_f32_e32 v54, v53
	s_nop 0
	v_add_u32_e32 v56, -1, v54
	v_fma_f32 v57, -v56, v54, v53
	v_cmp_ge_f32_e64 s[8:9], 0, v57
	v_add_u32_e32 v57, 1, v54
	s_nop 0
	v_cndmask_b32_e64 v56, v54, v56, s[8:9]
	v_fma_f32 v54, -v57, v54, v53
	v_cmp_lt_f32_e64 s[8:9], 0, v54
	s_nop 1
	v_cndmask_b32_e64 v54, v56, v57, s[8:9]
	v_mul_f32_e32 v56, 0x37800000, v54
	v_cndmask_b32_e32 v54, v54, v56, vcc
	v_cmp_class_f32_e32 vcc, v53, v41
	s_nop 1
	v_cndmask_b32_e32 v53, v54, v53, vcc
	v_div_scale_f32 v54, s[8:9], v53, v53, 1.0
	v_rcp_f32_e32 v56, v54
	s_nop 0
	v_fma_f32 v57, -v54, v56, 1.0
	v_fmac_f32_e32 v56, v57, v56
	v_div_scale_f32 v57, vcc, 1.0, v53, 1.0
	v_mul_f32_e32 v61, v57, v56
	v_fma_f32 v62, -v54, v61, v57
	v_fmac_f32_e32 v61, v62, v56
	v_fma_f32 v54, -v54, v61, v57
	v_div_fmas_f32 v54, v54, v56, v61
	v_div_fixup_f32 v61, v54, v53, 1.0
	v_mul_f32 v54, v3, v61
	v_mul_f32 v3, v4, v61
	v_mul_f32 v53, v52, v61
	v_mul_f32 v57, v58, v61
	v_mul_f32 v52, v55, v61
	v_mul_f32 v56, v59, v61
	v_mul_f32 v55, v60, v61
	v_mul_f32 v58, v2, v61
	s_branch .LBB0_11
